# tile-order decode: reciprocal estimate of the constant group size 8 replaced by its constant value (removes 40 VALU round trips at unit/phase starts), on top of loop rotation
# baseline (speedup 1.0000x reference)
;     __host__ __device__ bool next(int i, Unit& u) const {
;     ...
;         int wgid = (int)L; { const int q = nwg / NXCD, r = nwg % NXCD, xcd = wgid % NXCD, off = wgid / NXCD; wgid = (xcd < r ? xcd * (q + 1) : r * (q + 1) + (xcd - r) * q) + off; }
;         const int nig = WGM * nN, gid = wgid / nig, fm = gid * WGM, gsz = (nM - fm) < WGM ? (nM - fm) : WGM;
;         u.pm = fm + ((wgid % nig) % gsz); u.pn = (wgid % nig) / gsz; u.idx = i; return true;
; template <class Sched> __device__ __forceinline__ void stage_scales(PG8_LAS unsigned char* lds, const Sched& S, const float* rs, bool cols, int ldil, int tid) {
;     ...
;     if (tid < 256) { const int lper = 8 - ldil, c = tid, tm = ((c & ((1 << lper) - 1)) << ldil) + (c >> lper);
;         float eps = 1e-6f; asm volatile("" : "+s"(eps));
;         for (int i = 0; i < 16 && S.next(i, u); ++i) { const f32x4 a = *(const f32x4*)(rs + 4 * (size_t)(cols ? u.pn * BM + tm : u.pm * BM + tid));
;             tab[i * 256 + tid] = __builtin_amdgcn_rsqf(((a[0] + a[1]) + (a[2] + a[3])) * (1.0f / 1024.0f) + eps); } }
.LBB0_72:
	s_ashr_i32 s8, s10, 3
	s_add_i32 s8, s11, s8
	s_ashr_i32 s9, s8, 31
	s_lshr_b32 s9, s9, 26
	s_add_i32 s9, s8, s9
	s_ashr_i32 s10, s9, 6
	s_andn2_b32 s9, s9, 63
	s_sub_i32 s8, s8, s9
	s_lshl_b32 s9, s10, 3
	s_sub_i32 s10, 0x80, s9
	s_min_i32 s10, s10, 8
	s_abs_i32 s10, s10
	s_sub_i32 s14, 0, s10
	s_ashr_i32 s11, s8, 31
	s_abs_i32 s8, s8
	s_addk_i32 s13, 0x800
	v_add_u32_e32 v2, 0x24400, v2
	s_mov_b32 s15, 0x1fffffc0
	s_mul_i32 s14, s14, s15
	s_mul_hi_u32 s14, s15, s14
	s_add_i32 s15, s15, s14
	s_mul_hi_u32 s14, s8, s15
	s_mul_i32 s14, s14, s10
	s_sub_i32 s8, s8, s14
	s_sub_i32 s14, s8, s10
	s_cmp_ge_u32 s8, s10
	s_cselect_b32 s8, s14, s8
	s_sub_i32 s14, s8, s10
	s_cmp_ge_u32 s8, s10
	s_cselect_b32 s8, s14, s8
	s_xor_b32 s8, s8, s11
	s_sub_i32 s8, s8, s11
	s_add_i32 s9, s9, s8
	v_lshl_add_u32 v4, s9, 8, v0
	v_readlane_b32 s8, v254, 63
	v_ashrrev_i32_e32 v5, 31, v4
	v_readlane_b32 s9, v255, 0
	s_cmp_eq_u32 s13, 0
	s_cselect_b64 s[10:11], -1, 0
	v_lshl_add_u64 v[4:5], v[4:5], 4, s[8:9]
	global_load_dwordx4 v[4:7], v[4:5], off
	s_waitcnt vmcnt(0)
	v_mov_b32_e32 v8, v5
	v_mov_b32_e32 v9, v6
	v_mov_b32_e32 v5, v7
	v_pk_add_f32 v[4:5], v[8:9], v[4:5]
	s_nop 0
	v_add_f32_e32 v4, v4, v5
	v_mov_b32_e32 v5, s0
	v_fmamk_f32 v4, v4, 0x3a800000, v5
	v_rsq_f32_e32 v4, v4
	ds_write_b32 v2, v4

;     __host__ __device__ bool next(int i, Unit& u) const {
;     ...
;         int wgid = (int)L; { const int q = nwg / NXCD, r = nwg % NXCD, xcd = wgid % NXCD, off = wgid / NXCD; wgid = (xcd < r ? xcd * (q + 1) : r * (q + 1) + (xcd - r) * q) + off; }
;         const int nig = WGM * nN, gid = wgid / nig, fm = gid * WGM, gsz = (nM - fm) < WGM ? (nM - fm) : WGM;
;         u.pm = fm + ((wgid % nig) % gsz); u.pn = (wgid % nig) / gsz; u.idx = i; return true;
; template <class Sched> __device__ __forceinline__ void stage_scales(PG8_LAS unsigned char* lds, const Sched& S, const float* rs, bool cols, int ldil, int tid) {
;     ...
;     if (tid < 256) { const int lper = 8 - ldil, c = tid, tm = ((c & ((1 << lper) - 1)) << ldil) + (c >> lper);
;         float eps = 1e-6f; asm volatile("" : "+s"(eps));
;         for (int i = 0; i < 16 && S.next(i, u); ++i) { const f32x4 a = *(const f32x4*)(rs + 4 * (size_t)(cols ? u.pn * BM + tm : u.pm * BM + tid));
;             tab[i * 256 + tid] = __builtin_amdgcn_rsqf(((a[0] + a[1]) + (a[2] + a[3])) * (1.0f / 1024.0f) + eps); } }
.LBB0_79:
	s_ashr_i32 s6, s10, 3
	s_add_i32 s6, s14, s6
	s_ashr_i32 s7, s6, 31
	s_lshr_b32 s7, s7, 26
	s_add_i32 s7, s6, s7
	s_ashr_i32 s10, s7, 6
	s_andn2_b32 s7, s7, 63
	s_sub_i32 s6, s6, s7
	s_lshl_b32 s7, s10, 3
	s_sub_i32 s10, 0x80, s7
	s_min_i32 s10, s10, 8
	s_abs_i32 s10, s10
	s_sub_i32 s14, 0, s10
	s_ashr_i32 s11, s6, 31
	s_abs_i32 s6, s6
	s_nop 0
	s_mov_b32 s15, 0x1fffffc0
	s_mul_i32 s14, s14, s15
	s_mul_hi_u32 s14, s15, s14
	s_add_i32 s15, s15, s14
	s_mul_hi_u32 s14, s6, s15
	s_mul_i32 s14, s14, s10
	s_sub_i32 s6, s6, s14
	s_sub_i32 s14, s6, s10
	s_cmp_ge_u32 s6, s10
	s_cselect_b32 s6, s14, s6
	s_sub_i32 s14, s6, s10
	s_cmp_ge_u32 s6, s10
	s_cselect_b32 s6, s14, s6
	s_xor_b32 s6, s6, s11
	s_sub_i32 s6, s6, s11
	s_add_i32 s7, s7, s6
	v_lshl_add_u32 v4, s7, 8, v0
	v_readlane_b32 s6, v254, 63
	v_ashrrev_i32_e32 v5, 31, v4
	v_readlane_b32 s7, v255, 0
	s_nop 1
	v_lshl_add_u64 v[4:5], v[4:5], 4, s[6:7]
	global_load_dwordx4 v[4:7], v[4:5], off
	s_add_u32 s6, s8, s4
	s_addc_u32 s7, s9, s5
	s_add_u32 s10, s1, s6
	s_addc_u32 s11, s12, s7
	v_cmp_gt_i64_e32 vcc, s[10:11], v[238:239]
	s_mov_b64 s[10:11], -1
	s_and_b64 vcc, exec, vcc
	s_waitcnt vmcnt(0)
	v_mov_b32_e32 v8, v5
	v_mov_b32_e32 v9, v6
	v_mov_b32_e32 v5, v7
	v_pk_add_f32 v[4:5], v[8:9], v[4:5]
	s_nop 0
	v_add_f32_e32 v2, v4, v5
	v_mov_b32_e32 v4, s0
	v_fmamk_f32 v2, v2, 0x3a800000, v4
	v_rsq_f32_e32 v4, v2
	v_add_u32_e32 v2, s13, v1
	v_add_u32_e32 v5, 0x24000, v2
	ds_write_b32 v5, v4
	s_cbranch_vccnz .LBB0_73
	s_add_i32 s8, s88, s8
	s_ashr_i32 s9, s8, 31
	s_lshr_b32 s9, s9, 29
	s_add_i32 s10, s8, s9
	s_and_b32 s9, s10, -8
	s_sub_i32 s14, s8, s9
	s_cmp_lt_i32 s14, 0
	s_mov_b64 s[8:9], -1
	s_cbranch_scc1 .LBB0_82
	s_lshl_b32 s11, s14, 7
	s_mov_b64 s[8:9], 0

;     __host__ __device__ bool next(int i, Unit& u) const {
;     ...
;         int wgid = (int)L; { const int q = nwg / NXCD, r = nwg % NXCD, xcd = wgid % NXCD, off = wgid / NXCD; wgid = (xcd < r ? xcd * (q + 1) : r * (q + 1) + (xcd - r) * q) + off; }
;         const int nig = WGM * nN, gid = wgid / nig, fm = gid * WGM, gsz = (nM - fm) < WGM ? (nM - fm) : WGM;
;         u.pm = fm + ((wgid % nig) % gsz); u.pn = (wgid % nig) / gsz; u.idx = i; return true;
; template <class Epi, class Sched, bool ALIGN_EPI = false, bool SP2 = false>
; __device__ __forceinline__ void gemm_phase(PG8_LAS unsigned char* lds, const Gemm g, const Sched& S, const Epi& E, const int tid) {
;     ...
;         const bool has_next = S.next(ui + 1, nxt);
;         const char* nA = has_next ? (const char*)g.A + (size_t)nxt.pm * tstep : cA; const char* nB = has_next ? (const char*)g.Bt + (size_t)nxt.pn * tstep : cB;
.LBB0_99:
	s_ashr_i32 s12, s14, 3
	s_add_i32 s12, s36, s12
	s_ashr_i32 s13, s12, 31
	s_lshr_b32 s13, s13, 26
	s_add_i32 s13, s12, s13
	s_ashr_i32 s14, s13, 6
	s_lshl_b32 s14, s14, 3
	s_sub_i32 s15, 0x80, s14
	s_min_i32 s15, s15, 8
	s_abs_i32 s36, s15
	s_sub_i32 s41, 0, s36
	s_andn2_b32 s13, s13, 63
	s_sub_i32 s13, s12, s13
	s_abs_i32 s12, s13
	s_xor_b32 s37, s13, s15
	s_ashr_i32 s37, s37, 31
	s_mov_b32 s42, 0x1fffffc0
	s_mul_i32 s41, s41, s42
	s_mul_hi_u32 s41, s42, s41
	s_add_i32 s42, s42, s41
	s_mul_hi_u32 s41, s12, s42
	s_mul_i32 s42, s41, s36
	s_sub_i32 s12, s12, s42
	s_add_i32 s44, s41, 1
	s_sub_i32 s42, s12, s36
	s_cmp_ge_u32 s12, s36
	s_cselect_b32 s41, s44, s41
	s_cselect_b32 s12, s42, s12
	s_add_i32 s42, s41, 1
	s_cmp_ge_u32 s12, s36
	s_cselect_b32 s12, s42, s41
	s_xor_b32 s12, s12, s37
	s_sub_i32 s12, s12, s37
	s_mul_i32 s15, s12, s15
	s_sub_i32 s13, s13, s15
	s_add_i32 s14, s14, s13
	s_mov_b32 s41, s40

;     __host__ __device__ bool next(int i, Unit& u) const {
;     ...
;         int wgid = (int)L; { const int q = nwg / NXCD, r = nwg % NXCD, xcd = wgid % NXCD, off = wgid / NXCD; wgid = (xcd < r ? xcd * (q + 1) : r * (q + 1) + (xcd - r) * q) + off; }
;         const int nig = WGM * nN, gid = wgid / nig, fm = gid * WGM, gsz = (nM - fm) < WGM ? (nM - fm) : WGM;
;         u.pm = fm + ((wgid % nig) % gsz); u.pn = (wgid % nig) / gsz; u.idx = i; return true;
; template <class Sched> __device__ __forceinline__ void stage_scales(PG8_LAS unsigned char* lds, const Sched& S, const float* rs, bool cols, int ldil, int tid) {
;     ...
;     if (tid < 256) { const int lper = 8 - ldil, c = tid, tm = ((c & ((1 << lper) - 1)) << ldil) + (c >> lper);
;         float eps = 1e-6f; asm volatile("" : "+s"(eps));
;         for (int i = 0; i < 16 && S.next(i, u); ++i) { const f32x4 a = *(const f32x4*)(rs + 4 * (size_t)(cols ? u.pn * BM + tm : u.pm * BM + tid));
;             tab[i * 256 + tid] = __builtin_amdgcn_rsqf(((a[0] + a[1]) + (a[2] + a[3])) * (1.0f / 1024.0f) + eps); } }
.LBB0_269:
	s_and_b64 vcc, exec, s[2:3]
	s_cbranch_vccz .LBB0_305
	v_readlane_b32 s18, v254, 59
	s_cmp_gt_i32 s18, 1
	s_cbranch_scc0 .LBB0_306
	s_mov_b64 s[20:21], s[16:17]
	s_cmp_gt_i32 s18, 3
	s_mov_b64 s[2:3], -1
	s_movk_i32 s17, 0xc1
	s_cbranch_scc0 .LBB0_309
	v_mbcnt_lo_u32_b32 v2, -1, 0
	v_mbcnt_hi_u32_b32 v2, -1, v2
	s_movk_i32 s0, 0x100
	v_add_u32_e32 v1, s30, v2
	v_cmp_gt_i32_e32 vcc, s0, v1
	s_and_saveexec_b64 s[2:3], vcc
	s_cbranch_execz .LBB0_290
	s_mov_b32 s6, 0x358637bd
	s_cmpk_gt_i32 s90, 0x5ff
	s_cbranch_scc1 .LBB0_290
	s_ashr_i32 s0, s90, 31
	s_lshr_b32 s1, s0, 29
	s_add_i32 s1, s90, s1
	s_ashr_i32 s4, s1, 3
	s_and_b32 s1, s1, -8
	s_ashr_i32 s7, s88, 31
	s_sub_i32 s1, s90, s1
	s_cmp_lt_i32 s1, 0
	s_cselect_b32 s5, s17, 0xc0
	s_mul_i32 s1, s1, s5
	s_add_i32 s1, s1, s4
	s_mul_hi_i32 s4, s1, 0x2aaaaaab
	s_lshr_b32 s5, s4, 31
	s_ashr_i32 s4, s4, 4
	s_add_i32 s4, s4, s5
	s_mul_i32 s5, s4, 0x60
	s_lshl_b32 s4, s4, 3
	s_sub_i32 s1, s1, s5
	s_sub_i32 s5, 0x80, s4
	s_min_i32 s5, s5, 8
	s_abs_i32 s5, s5
	s_sub_i32 s9, 0, s5
	s_ashr_i32 s8, s1, 31
	s_abs_i32 s1, s1
	v_lshl_add_u32 v0, v1, 2, 0
	v_add_u32_e32 v0, 0x20000, v0
	s_mov_b32 s10, 0x1fffffc0
	s_mul_i32 s9, s9, s10
	s_mul_hi_u32 s9, s10, s9
	s_add_i32 s10, s10, s9
	s_mul_hi_u32 s9, s1, s10
	s_mul_i32 s9, s9, s5
	s_sub_i32 s1, s1, s9
	s_sub_i32 s9, s1, s5
	s_cmp_ge_u32 s1, s5
	s_cselect_b32 s1, s9, s1
	s_sub_i32 s9, s1, s5
	s_cmp_ge_u32 s1, s5
	s_cselect_b32 s1, s9, s1
	s_xor_b32 s1, s1, s8
	s_sub_i32 s1, s1, s8
	s_add_i32 s4, s4, s1
	v_lshl_add_u32 v4, s4, 8, v1
	v_readlane_b32 s4, v254, 63
	v_ashrrev_i32_e32 v5, 31, v4
	v_readlane_b32 s5, v255, 0
	s_nop 1
	v_lshl_add_u64 v[4:5], v[4:5], 4, s[4:5]
	global_load_dwordx4 v[64:67], v[4:5], off
	s_add_u32 s4, s88, s90
	s_addc_u32 s5, s7, s0
	v_cmp_gt_i64_e32 vcc, s[4:5], v[252:253]
	s_and_b64 vcc, exec, vcc
	s_cbranch_vccnz .LBB0_290
	s_ashr_i32 s0, s4, 31
	s_lshr_b32 s0, s0, 29
	s_add_i32 s0, s4, s0
	s_ashr_i32 s1, s0, 3
	s_and_b32 s0, s0, -8
	s_sub_i32 s0, s4, s0
	s_cmp_lt_i32 s0, 0
	s_cselect_b32 s8, s17, 0xc0
	s_mul_i32 s0, s0, s8
	s_add_i32 s0, s0, s1
	s_mul_hi_i32 s1, s0, 0x2aaaaaab
	s_lshr_b32 s8, s1, 31
	s_ashr_i32 s1, s1, 4
	s_add_i32 s1, s1, s8
	s_mul_i32 s8, s1, 0x60
	s_lshl_b32 s1, s1, 3
	s_sub_i32 s0, s0, s8
	s_sub_i32 s8, 0x80, s1
	s_min_i32 s8, s8, 8
	s_abs_i32 s8, s8
	s_sub_i32 s10, 0, s8
	s_ashr_i32 s9, s0, 31
	s_abs_i32 s0, s0
	s_nop 0
	s_mov_b32 s11, 0x1fffffc0
	s_mul_i32 s10, s10, s11
	s_mul_hi_u32 s10, s11, s10
	s_add_i32 s11, s11, s10
	s_mul_hi_u32 s10, s0, s11
	s_mul_i32 s10, s10, s8
	s_sub_i32 s0, s0, s10
	s_sub_i32 s10, s0, s8
	s_cmp_ge_u32 s0, s8
	s_cselect_b32 s0, s10, s0
	s_sub_i32 s10, s0, s8
	s_cmp_ge_u32 s0, s8
	s_cselect_b32 s0, s10, s0
	s_xor_b32 s0, s0, s9
	s_sub_i32 s0, s0, s9
	s_add_i32 s1, s1, s0
	v_lshl_add_u32 v4, s1, 8, v1
	v_readlane_b32 s0, v254, 63
	v_ashrrev_i32_e32 v5, 31, v4
	v_readlane_b32 s1, v255, 0
	s_add_u32 s4, s4, s88
	s_addc_u32 s5, s5, s7
	v_lshl_add_u64 v[4:5], v[4:5], 4, s[0:1]
	global_load_dwordx4 v[68:71], v[4:5], off
	v_cmp_gt_i64_e32 vcc, s[4:5], v[252:253]
	s_and_b64 vcc, exec, vcc
	s_cbranch_vccnz .LBB0_290
	s_ashr_i32 s0, s4, 31
	s_lshr_b32 s0, s0, 29
	s_add_i32 s0, s4, s0
	s_ashr_i32 s1, s0, 3
	s_and_b32 s0, s0, -8
	s_sub_i32 s0, s4, s0
	s_cmp_lt_i32 s0, 0
	s_cselect_b32 s8, s17, 0xc0
	s_mul_i32 s0, s0, s8
	s_add_i32 s0, s0, s1
	s_mul_hi_i32 s1, s0, 0x2aaaaaab
	s_lshr_b32 s8, s1, 31
	s_ashr_i32 s1, s1, 4
	s_add_i32 s1, s1, s8
	s_mul_i32 s8, s1, 0x60
	s_lshl_b32 s1, s1, 3
	s_sub_i32 s0, s0, s8
	s_sub_i32 s8, 0x80, s1
	s_min_i32 s8, s8, 8
	s_abs_i32 s8, s8
	s_sub_i32 s10, 0, s8
	s_ashr_i32 s9, s0, 31
	s_abs_i32 s0, s0
	s_nop 0
	s_mov_b32 s11, 0x1fffffc0
	s_mul_i32 s10, s10, s11
	s_mul_hi_u32 s10, s11, s10
	s_add_i32 s11, s11, s10
	s_mul_hi_u32 s10, s0, s11
	s_mul_i32 s10, s10, s8
	s_sub_i32 s0, s0, s10
	s_sub_i32 s10, s0, s8
	s_cmp_ge_u32 s0, s8
	s_cselect_b32 s0, s10, s0
	s_sub_i32 s10, s0, s8
	s_cmp_ge_u32 s0, s8
	s_cselect_b32 s0, s10, s0
	s_xor_b32 s0, s0, s9
	s_sub_i32 s0, s0, s9
	s_add_i32 s1, s1, s0
	v_lshl_add_u32 v4, s1, 8, v1
	v_readlane_b32 s0, v254, 63
	v_ashrrev_i32_e32 v5, 31, v4
	v_readlane_b32 s1, v255, 0
	s_add_u32 s4, s4, s88
	s_addc_u32 s5, s5, s7
	v_lshl_add_u64 v[4:5], v[4:5], 4, s[0:1]
	global_load_dwordx4 v[72:75], v[4:5], off
	v_cmp_gt_i64_e32 vcc, s[4:5], v[252:253]
	s_and_b64 vcc, exec, vcc
	s_cbranch_vccnz .LBB0_290
	s_ashr_i32 s0, s4, 31
	s_lshr_b32 s0, s0, 29
	s_add_i32 s0, s4, s0
	s_ashr_i32 s1, s0, 3
	s_and_b32 s0, s0, -8
	s_sub_i32 s0, s4, s0
	s_cmp_lt_i32 s0, 0
	s_cselect_b32 s8, s17, 0xc0
	s_mul_i32 s0, s0, s8
	s_add_i32 s0, s0, s1
	s_mul_hi_i32 s1, s0, 0x2aaaaaab
	s_lshr_b32 s8, s1, 31
	s_ashr_i32 s1, s1, 4
	s_add_i32 s1, s1, s8
	s_mul_i32 s8, s1, 0x60
	s_lshl_b32 s1, s1, 3
	s_sub_i32 s0, s0, s8
	s_sub_i32 s8, 0x80, s1
	s_min_i32 s8, s8, 8
	s_abs_i32 s8, s8
	s_sub_i32 s10, 0, s8
	s_ashr_i32 s9, s0, 31
	s_abs_i32 s0, s0
	s_nop 0
	s_mov_b32 s11, 0x1fffffc0
	s_mul_i32 s10, s10, s11
	s_mul_hi_u32 s10, s11, s10
	s_add_i32 s11, s11, s10
	s_mul_hi_u32 s10, s0, s11
	s_mul_i32 s10, s10, s8
	s_sub_i32 s0, s0, s10
	s_sub_i32 s10, s0, s8
	s_cmp_ge_u32 s0, s8
	s_cselect_b32 s0, s10, s0
	s_sub_i32 s10, s0, s8
	s_cmp_ge_u32 s0, s8
	s_cselect_b32 s0, s10, s0
	s_xor_b32 s0, s0, s9
	s_sub_i32 s0, s0, s9
	s_add_i32 s1, s1, s0
	v_lshl_add_u32 v4, s1, 8, v1
	v_readlane_b32 s0, v254, 63
	v_ashrrev_i32_e32 v5, 31, v4
	v_readlane_b32 s1, v255, 0
	s_add_u32 s4, s4, s88
	s_addc_u32 s5, s5, s7
	v_lshl_add_u64 v[4:5], v[4:5], 4, s[0:1]
	global_load_dwordx4 v[76:79], v[4:5], off
	v_cmp_gt_i64_e32 vcc, s[4:5], v[252:253]
	s_and_b64 vcc, exec, vcc
	s_cbranch_vccnz .LBB0_290
;     __host__ __device__ bool next(int i, Unit& u) const {
;         const long L = (long)i * G + c; if (L >= nwg) return false;
;         int wgid = (int)L; { const int q = nwg / NXCD, r = nwg % NXCD, xcd = wgid % NXCD, off = wgid / NXCD; wgid = (xcd < r ? xcd * (q + 1) : r * (q + 1) + (xcd - r) * q) + off; }
;         const int nig = WGM * nN, gid = wgid / nig, fm = gid * WGM, gsz = (nM - fm) < WGM ? (nM - fm) : WGM;
;         u.pm = fm + ((wgid % nig) % gsz); u.pn = (wgid % nig) / gsz; u.idx = i; return true;
; template <class Sched> __device__ __forceinline__ void stage_scales(PG8_LAS unsigned char* lds, const Sched& S, const float* rs, bool cols, int ldil, int tid) {
;     ...
;         for (int i = 0; i < 16 && S.next(i, u); ++i) { const f32x4 a = *(const f32x4*)(rs + 4 * (size_t)(cols ? u.pn * BM + tm : u.pm * BM + tid));
;             tab[i * 256 + tid] = __builtin_amdgcn_rsqf(((a[0] + a[1]) + (a[2] + a[3])) * (1.0f / 1024.0f) + eps); } }
	s_ashr_i32 s0, s4, 31
	s_lshr_b32 s0, s0, 29
	s_add_i32 s0, s4, s0
	s_ashr_i32 s1, s0, 3
	s_and_b32 s0, s0, -8
	s_sub_i32 s0, s4, s0
	s_cmp_lt_i32 s0, 0
	s_cselect_b32 s8, s17, 0xc0
	s_mul_i32 s0, s0, s8
	s_add_i32 s0, s0, s1
	s_mul_hi_i32 s1, s0, 0x2aaaaaab
	s_lshr_b32 s8, s1, 31
	s_ashr_i32 s1, s1, 4
	s_add_i32 s1, s1, s8
	s_mul_i32 s8, s1, 0x60
	s_lshl_b32 s1, s1, 3
	s_sub_i32 s0, s0, s8
	s_sub_i32 s8, 0x80, s1
	s_min_i32 s8, s8, 8
	s_abs_i32 s8, s8
	s_sub_i32 s10, 0, s8
	s_ashr_i32 s9, s0, 31
	s_abs_i32 s0, s0
	s_nop 0
	s_mov_b32 s11, 0x1fffffc0
	s_mul_i32 s10, s10, s11
	s_mul_hi_u32 s10, s11, s10
	s_add_i32 s11, s11, s10
	s_mul_hi_u32 s10, s0, s11
	s_mul_i32 s10, s10, s8
	s_sub_i32 s0, s0, s10
	s_sub_i32 s10, s0, s8
	s_cmp_ge_u32 s0, s8
	s_cselect_b32 s0, s10, s0
	s_sub_i32 s10, s0, s8
	s_cmp_ge_u32 s0, s8
	s_cselect_b32 s0, s10, s0
	s_xor_b32 s0, s0, s9
	s_sub_i32 s0, s0, s9
	s_add_i32 s1, s1, s0
	v_lshl_add_u32 v4, s1, 8, v1
	v_readlane_b32 s0, v254, 63
	v_ashrrev_i32_e32 v5, 31, v4
	v_readlane_b32 s1, v255, 0
	s_add_u32 s4, s4, s88
	s_addc_u32 s5, s5, s7
	v_lshl_add_u64 v[4:5], v[4:5], 4, s[0:1]
	global_load_dwordx4 v[80:83], v[4:5], off
	v_cmp_gt_i64_e32 vcc, s[4:5], v[252:253]
	s_and_b64 vcc, exec, vcc
	s_cbranch_vccnz .LBB0_290
	s_ashr_i32 s0, s4, 31
	s_lshr_b32 s0, s0, 29
	s_add_i32 s0, s4, s0
	s_ashr_i32 s1, s0, 3
	s_and_b32 s0, s0, -8
	s_sub_i32 s0, s4, s0
	s_cmp_lt_i32 s0, 0
	s_cselect_b32 s8, s17, 0xc0
	s_mul_i32 s0, s0, s8
	s_add_i32 s0, s0, s1
	s_mul_hi_i32 s1, s0, 0x2aaaaaab
	s_lshr_b32 s8, s1, 31
	s_ashr_i32 s1, s1, 4
	s_add_i32 s1, s1, s8
	s_mul_i32 s8, s1, 0x60
	s_lshl_b32 s1, s1, 3
	s_sub_i32 s0, s0, s8
	s_sub_i32 s8, 0x80, s1
	s_min_i32 s8, s8, 8
	s_abs_i32 s8, s8
	s_sub_i32 s10, 0, s8
	s_ashr_i32 s9, s0, 31
	s_abs_i32 s0, s0
	s_nop 0
	s_mov_b32 s11, 0x1fffffc0
	s_mul_i32 s10, s10, s11
	s_mul_hi_u32 s10, s11, s10
	s_add_i32 s11, s11, s10
	s_mul_hi_u32 s10, s0, s11
	s_mul_i32 s10, s10, s8
	s_sub_i32 s0, s0, s10
	s_sub_i32 s10, s0, s8
	s_cmp_ge_u32 s0, s8
	s_cselect_b32 s0, s10, s0
	s_sub_i32 s10, s0, s8
	s_cmp_ge_u32 s0, s8
	s_cselect_b32 s0, s10, s0
	s_xor_b32 s0, s0, s9
	s_sub_i32 s0, s0, s9
	s_add_i32 s1, s1, s0
	v_lshl_add_u32 v4, s1, 8, v1
	v_readlane_b32 s0, v254, 63
	v_ashrrev_i32_e32 v5, 31, v4
	v_readlane_b32 s1, v255, 0
	s_add_u32 s4, s4, s88
	s_addc_u32 s5, s5, s7
	v_lshl_add_u64 v[4:5], v[4:5], 4, s[0:1]
	global_load_dwordx4 v[84:87], v[4:5], off
	v_cmp_gt_i64_e32 vcc, s[4:5], v[252:253]
	s_and_b64 vcc, exec, vcc
	s_cbranch_vccnz .LBB0_290
	s_ashr_i32 s0, s4, 31
	s_lshr_b32 s0, s0, 29
	s_add_i32 s0, s4, s0
	s_ashr_i32 s1, s0, 3
	s_and_b32 s0, s0, -8
	s_sub_i32 s0, s4, s0
	s_cmp_lt_i32 s0, 0
	s_cselect_b32 s8, s17, 0xc0
	s_mul_i32 s0, s0, s8
	s_add_i32 s0, s0, s1
	s_mul_hi_i32 s1, s0, 0x2aaaaaab
	s_lshr_b32 s8, s1, 31
	s_ashr_i32 s1, s1, 4
	s_add_i32 s1, s1, s8
	s_mul_i32 s8, s1, 0x60
	s_lshl_b32 s1, s1, 3
	s_sub_i32 s0, s0, s8
	s_sub_i32 s8, 0x80, s1
	s_min_i32 s8, s8, 8
	s_abs_i32 s8, s8
	s_sub_i32 s10, 0, s8
	s_ashr_i32 s9, s0, 31
	s_abs_i32 s0, s0
	s_nop 0
	s_mov_b32 s11, 0x1fffffc0
	s_mul_i32 s10, s10, s11
	s_mul_hi_u32 s10, s11, s10
	s_add_i32 s11, s11, s10
	s_mul_hi_u32 s10, s0, s11
	s_mul_i32 s10, s10, s8
	s_sub_i32 s0, s0, s10
	s_sub_i32 s10, s0, s8
	s_cmp_ge_u32 s0, s8
	s_cselect_b32 s0, s10, s0
	s_sub_i32 s10, s0, s8
	s_cmp_ge_u32 s0, s8
	s_cselect_b32 s0, s10, s0
	s_xor_b32 s0, s0, s9
	s_sub_i32 s0, s0, s9
	s_add_i32 s1, s1, s0
	v_lshl_add_u32 v4, s1, 8, v1
	v_readlane_b32 s0, v254, 63
	v_ashrrev_i32_e32 v5, 31, v4
	v_readlane_b32 s1, v255, 0
	s_add_u32 s4, s4, s88
	s_addc_u32 s5, s5, s7
	v_lshl_add_u64 v[4:5], v[4:5], 4, s[0:1]
	global_load_dwordx4 v[88:91], v[4:5], off
	v_cmp_gt_i64_e32 vcc, s[4:5], v[252:253]
	s_and_b64 vcc, exec, vcc
	s_cbranch_vccnz .LBB0_290
	s_ashr_i32 s0, s4, 31
	s_lshr_b32 s0, s0, 29
	s_add_i32 s0, s4, s0
	s_ashr_i32 s1, s0, 3
	s_and_b32 s0, s0, -8
	s_sub_i32 s0, s4, s0
	s_cmp_lt_i32 s0, 0
	s_cselect_b32 s8, s17, 0xc0
	s_mul_i32 s0, s0, s8
	s_add_i32 s0, s0, s1
	s_mul_hi_i32 s1, s0, 0x2aaaaaab
	s_lshr_b32 s8, s1, 31
	s_ashr_i32 s1, s1, 4
	s_add_i32 s1, s1, s8
	s_mul_i32 s8, s1, 0x60
	s_lshl_b32 s1, s1, 3
	s_sub_i32 s0, s0, s8
	s_sub_i32 s8, 0x80, s1
	s_min_i32 s8, s8, 8
	s_abs_i32 s8, s8
	s_sub_i32 s10, 0, s8
	s_ashr_i32 s9, s0, 31
	s_abs_i32 s0, s0
	s_nop 0
	s_mov_b32 s11, 0x1fffffc0
	s_mul_i32 s10, s10, s11
	s_mul_hi_u32 s10, s11, s10
	s_add_i32 s11, s11, s10
	s_mul_hi_u32 s10, s0, s11
	s_mul_i32 s10, s10, s8
	s_sub_i32 s0, s0, s10
	s_sub_i32 s10, s0, s8
	s_cmp_ge_u32 s0, s8
	s_cselect_b32 s0, s10, s0
	s_sub_i32 s10, s0, s8
	s_cmp_ge_u32 s0, s8
	s_cselect_b32 s0, s10, s0
	s_xor_b32 s0, s0, s9
	s_sub_i32 s0, s0, s9
	s_add_i32 s1, s1, s0
	v_lshl_add_u32 v4, s1, 8, v1
	v_readlane_b32 s0, v254, 63
	v_ashrrev_i32_e32 v5, 31, v4
	v_readlane_b32 s1, v255, 0
	s_add_u32 s4, s4, s88
	s_addc_u32 s5, s5, s7
	v_lshl_add_u64 v[4:5], v[4:5], 4, s[0:1]
	global_load_dwordx4 v[92:95], v[4:5], off
	v_cmp_gt_i64_e32 vcc, s[4:5], v[252:253]
	s_and_b64 vcc, exec, vcc
	s_cbranch_vccnz .LBB0_290
;     __host__ __device__ bool next(int i, Unit& u) const {
;         const long L = (long)i * G + c; if (L >= nwg) return false;
;         int wgid = (int)L; { const int q = nwg / NXCD, r = nwg % NXCD, xcd = wgid % NXCD, off = wgid / NXCD; wgid = (xcd < r ? xcd * (q + 1) : r * (q + 1) + (xcd - r) * q) + off; }
;         const int nig = WGM * nN, gid = wgid / nig, fm = gid * WGM, gsz = (nM - fm) < WGM ? (nM - fm) : WGM;
;         u.pm = fm + ((wgid % nig) % gsz); u.pn = (wgid % nig) / gsz; u.idx = i; return true;
; template <class Sched> __device__ __forceinline__ void stage_scales(PG8_LAS unsigned char* lds, const Sched& S, const float* rs, bool cols, int ldil, int tid) {
;     ...
;         for (int i = 0; i < 16 && S.next(i, u); ++i) { const f32x4 a = *(const f32x4*)(rs + 4 * (size_t)(cols ? u.pn * BM + tm : u.pm * BM + tid));
;             tab[i * 256 + tid] = __builtin_amdgcn_rsqf(((a[0] + a[1]) + (a[2] + a[3])) * (1.0f / 1024.0f) + eps); } }
	s_ashr_i32 s0, s4, 31
	s_lshr_b32 s0, s0, 29
	s_add_i32 s0, s4, s0
	s_ashr_i32 s1, s0, 3
	s_and_b32 s0, s0, -8
	s_sub_i32 s0, s4, s0
	s_cmp_lt_i32 s0, 0
	s_cselect_b32 s8, s17, 0xc0
	s_mul_i32 s0, s0, s8
	s_add_i32 s0, s0, s1
	s_mul_hi_i32 s1, s0, 0x2aaaaaab
	s_lshr_b32 s8, s1, 31
	s_ashr_i32 s1, s1, 4
	s_add_i32 s1, s1, s8
	s_mul_i32 s8, s1, 0x60
	s_lshl_b32 s1, s1, 3
	s_sub_i32 s0, s0, s8
	s_sub_i32 s8, 0x80, s1
	s_min_i32 s8, s8, 8
	s_abs_i32 s8, s8
	s_sub_i32 s10, 0, s8
	s_ashr_i32 s9, s0, 31
	s_abs_i32 s0, s0
	s_nop 0
	s_mov_b32 s11, 0x1fffffc0
	s_mul_i32 s10, s10, s11
	s_mul_hi_u32 s10, s11, s10
	s_add_i32 s11, s11, s10
	s_mul_hi_u32 s10, s0, s11
	s_mul_i32 s10, s10, s8
	s_sub_i32 s0, s0, s10
	s_sub_i32 s10, s0, s8
	s_cmp_ge_u32 s0, s8
	s_cselect_b32 s0, s10, s0
	s_sub_i32 s10, s0, s8
	s_cmp_ge_u32 s0, s8
	s_cselect_b32 s0, s10, s0
	s_xor_b32 s0, s0, s9
	s_sub_i32 s0, s0, s9
	s_add_i32 s1, s1, s0
	v_lshl_add_u32 v4, s1, 8, v1
	v_readlane_b32 s0, v254, 63
	v_ashrrev_i32_e32 v5, 31, v4
	v_readlane_b32 s1, v255, 0
	s_add_u32 s4, s4, s88
	s_addc_u32 s5, s5, s7
	v_lshl_add_u64 v[4:5], v[4:5], 4, s[0:1]
	global_load_dwordx4 v[96:99], v[4:5], off
	v_cmp_gt_i64_e32 vcc, s[4:5], v[252:253]
	s_and_b64 vcc, exec, vcc
	s_cbranch_vccnz .LBB0_290
	s_ashr_i32 s0, s4, 31
	s_lshr_b32 s0, s0, 29
	s_add_i32 s0, s4, s0
	s_ashr_i32 s1, s0, 3
	s_and_b32 s0, s0, -8
	s_sub_i32 s0, s4, s0
	s_cmp_lt_i32 s0, 0
	s_cselect_b32 s8, s17, 0xc0
	s_mul_i32 s0, s0, s8
	s_add_i32 s0, s0, s1
	s_mul_hi_i32 s1, s0, 0x2aaaaaab
	s_lshr_b32 s8, s1, 31
	s_ashr_i32 s1, s1, 4
	s_add_i32 s1, s1, s8
	s_mul_i32 s8, s1, 0x60
	s_lshl_b32 s1, s1, 3
	s_sub_i32 s0, s0, s8
	s_sub_i32 s8, 0x80, s1
	s_min_i32 s8, s8, 8
	s_abs_i32 s8, s8
	s_sub_i32 s10, 0, s8
	s_ashr_i32 s9, s0, 31
	s_abs_i32 s0, s0
	s_nop 0
	s_mov_b32 s11, 0x1fffffc0
	s_mul_i32 s10, s10, s11
	s_mul_hi_u32 s10, s11, s10
	s_add_i32 s11, s11, s10
	s_mul_hi_u32 s10, s0, s11
	s_mul_i32 s10, s10, s8
	s_sub_i32 s0, s0, s10
	s_sub_i32 s10, s0, s8
	s_cmp_ge_u32 s0, s8
	s_cselect_b32 s0, s10, s0
	s_sub_i32 s10, s0, s8
	s_cmp_ge_u32 s0, s8
	s_cselect_b32 s0, s10, s0
	s_xor_b32 s0, s0, s9
	s_sub_i32 s0, s0, s9
	s_add_i32 s1, s1, s0
	v_lshl_add_u32 v4, s1, 8, v1
	v_readlane_b32 s0, v254, 63
	v_ashrrev_i32_e32 v5, 31, v4
	v_readlane_b32 s1, v255, 0
	s_add_u32 s4, s4, s88
	s_addc_u32 s5, s5, s7
	v_lshl_add_u64 v[4:5], v[4:5], 4, s[0:1]
	global_load_dwordx4 v[100:103], v[4:5], off
	v_cmp_gt_i64_e32 vcc, s[4:5], v[252:253]
	s_and_b64 vcc, exec, vcc
	s_cbranch_vccnz .LBB0_290
	s_ashr_i32 s0, s4, 31
	s_lshr_b32 s0, s0, 29
	s_add_i32 s0, s4, s0
	s_ashr_i32 s1, s0, 3
	s_and_b32 s0, s0, -8
	s_sub_i32 s0, s4, s0
	s_cmp_lt_i32 s0, 0
	s_cselect_b32 s8, s17, 0xc0
	s_mul_i32 s0, s0, s8
	s_add_i32 s0, s0, s1
	s_mul_hi_i32 s1, s0, 0x2aaaaaab
	s_lshr_b32 s8, s1, 31
	s_ashr_i32 s1, s1, 4
	s_add_i32 s1, s1, s8
	s_mul_i32 s8, s1, 0x60
	s_lshl_b32 s1, s1, 3
	s_sub_i32 s0, s0, s8
	s_sub_i32 s8, 0x80, s1
	s_min_i32 s8, s8, 8
	s_abs_i32 s8, s8
	s_sub_i32 s10, 0, s8
	s_ashr_i32 s9, s0, 31
	s_abs_i32 s0, s0
	s_nop 0
	s_mov_b32 s11, 0x1fffffc0
	s_mul_i32 s10, s10, s11
	s_mul_hi_u32 s10, s11, s10
	s_add_i32 s11, s11, s10
	s_mul_hi_u32 s10, s0, s11
	s_mul_i32 s10, s10, s8
	s_sub_i32 s0, s0, s10
	s_sub_i32 s10, s0, s8
	s_cmp_ge_u32 s0, s8
	s_cselect_b32 s0, s10, s0
	s_sub_i32 s10, s0, s8
	s_cmp_ge_u32 s0, s8
	s_cselect_b32 s0, s10, s0
	s_xor_b32 s0, s0, s9
	s_sub_i32 s0, s0, s9
	s_add_i32 s1, s1, s0
	v_lshl_add_u32 v4, s1, 8, v1
	v_readlane_b32 s0, v254, 63
	v_ashrrev_i32_e32 v5, 31, v4
	v_readlane_b32 s1, v255, 0
	s_add_u32 s4, s4, s88
	s_addc_u32 s5, s5, s7
	v_lshl_add_u64 v[4:5], v[4:5], 4, s[0:1]
	global_load_dwordx4 v[104:107], v[4:5], off
	v_cmp_gt_i64_e32 vcc, s[4:5], v[252:253]
	s_and_b64 vcc, exec, vcc
	s_cbranch_vccnz .LBB0_290
	s_ashr_i32 s0, s4, 31
	s_lshr_b32 s0, s0, 29
	s_add_i32 s0, s4, s0
	s_ashr_i32 s1, s0, 3
	s_and_b32 s0, s0, -8
	s_sub_i32 s0, s4, s0
	s_cmp_lt_i32 s0, 0
	s_cselect_b32 s8, s17, 0xc0
	s_mul_i32 s0, s0, s8
	s_add_i32 s0, s0, s1
	s_mul_hi_i32 s1, s0, 0x2aaaaaab
	s_lshr_b32 s8, s1, 31
	s_ashr_i32 s1, s1, 4
	s_add_i32 s1, s1, s8
	s_mul_i32 s8, s1, 0x60
	s_lshl_b32 s1, s1, 3
	s_sub_i32 s0, s0, s8
	s_sub_i32 s8, 0x80, s1
	s_min_i32 s8, s8, 8
	s_abs_i32 s8, s8
	s_sub_i32 s10, 0, s8
	s_ashr_i32 s9, s0, 31
	s_abs_i32 s0, s0
	s_nop 0
	s_mov_b32 s11, 0x1fffffc0
	s_mul_i32 s10, s10, s11
	s_mul_hi_u32 s10, s11, s10
	s_add_i32 s11, s11, s10
	s_mul_hi_u32 s10, s0, s11
	s_mul_i32 s10, s10, s8
	s_sub_i32 s0, s0, s10
	s_sub_i32 s10, s0, s8
	s_cmp_ge_u32 s0, s8
	s_cselect_b32 s0, s10, s0
	s_sub_i32 s10, s0, s8
	s_cmp_ge_u32 s0, s8
	s_cselect_b32 s0, s10, s0
	s_xor_b32 s0, s0, s9
	s_sub_i32 s0, s0, s9
	s_add_i32 s1, s1, s0
	v_lshl_add_u32 v4, s1, 8, v1
	v_readlane_b32 s0, v254, 63
	v_ashrrev_i32_e32 v5, 31, v4
	v_readlane_b32 s1, v255, 0
	s_add_u32 s4, s4, s88
	s_addc_u32 s5, s5, s7
	v_lshl_add_u64 v[4:5], v[4:5], 4, s[0:1]
	global_load_dwordx4 v[108:111], v[4:5], off
	v_cmp_gt_i64_e32 vcc, s[4:5], v[252:253]
	s_and_b64 vcc, exec, vcc
	s_cbranch_vccnz .LBB0_290
;     __host__ __device__ bool next(int i, Unit& u) const {
;         const long L = (long)i * G + c; if (L >= nwg) return false;
;         int wgid = (int)L; { const int q = nwg / NXCD, r = nwg % NXCD, xcd = wgid % NXCD, off = wgid / NXCD; wgid = (xcd < r ? xcd * (q + 1) : r * (q + 1) + (xcd - r) * q) + off; }
;         const int nig = WGM * nN, gid = wgid / nig, fm = gid * WGM, gsz = (nM - fm) < WGM ? (nM - fm) : WGM;
;         u.pm = fm + ((wgid % nig) % gsz); u.pn = (wgid % nig) / gsz; u.idx = i; return true;
; template <class Sched> __device__ __forceinline__ void stage_scales(PG8_LAS unsigned char* lds, const Sched& S, const float* rs, bool cols, int ldil, int tid) {
;     ...
;         for (int i = 0; i < 16 && S.next(i, u); ++i) { const f32x4 a = *(const f32x4*)(rs + 4 * (size_t)(cols ? u.pn * BM + tm : u.pm * BM + tid));
;             tab[i * 256 + tid] = __builtin_amdgcn_rsqf(((a[0] + a[1]) + (a[2] + a[3])) * (1.0f / 1024.0f) + eps); } }
	s_ashr_i32 s0, s4, 31
	s_lshr_b32 s0, s0, 29
	s_add_i32 s0, s4, s0
	s_ashr_i32 s1, s0, 3
	s_and_b32 s0, s0, -8
	s_sub_i32 s0, s4, s0
	s_cmp_lt_i32 s0, 0
	s_cselect_b32 s8, s17, 0xc0
	s_mul_i32 s0, s0, s8
	s_add_i32 s0, s0, s1
	s_mul_hi_i32 s1, s0, 0x2aaaaaab
	s_lshr_b32 s8, s1, 31
	s_ashr_i32 s1, s1, 4
	s_add_i32 s1, s1, s8
	s_mul_i32 s8, s1, 0x60
	s_lshl_b32 s1, s1, 3
	s_sub_i32 s0, s0, s8
	s_sub_i32 s8, 0x80, s1
	s_min_i32 s8, s8, 8
	s_abs_i32 s8, s8
	s_sub_i32 s10, 0, s8
	s_ashr_i32 s9, s0, 31
	s_abs_i32 s0, s0
	s_nop 0
	s_mov_b32 s11, 0x1fffffc0
	s_mul_i32 s10, s10, s11
	s_mul_hi_u32 s10, s11, s10
	s_add_i32 s11, s11, s10
	s_mul_hi_u32 s10, s0, s11
	s_mul_i32 s10, s10, s8
	s_sub_i32 s0, s0, s10
	s_sub_i32 s10, s0, s8
	s_cmp_ge_u32 s0, s8
	s_cselect_b32 s0, s10, s0
	s_sub_i32 s10, s0, s8
	s_cmp_ge_u32 s0, s8
	s_cselect_b32 s0, s10, s0
	s_xor_b32 s0, s0, s9
	s_sub_i32 s0, s0, s9
	s_add_i32 s1, s1, s0
	v_lshl_add_u32 v4, s1, 8, v1
	v_readlane_b32 s0, v254, 63
	v_ashrrev_i32_e32 v5, 31, v4
	v_readlane_b32 s1, v255, 0
	s_add_u32 s4, s4, s88
	s_addc_u32 s5, s5, s7
	v_lshl_add_u64 v[4:5], v[4:5], 4, s[0:1]
	global_load_dwordx4 v[112:115], v[4:5], off
	v_cmp_gt_i64_e32 vcc, s[4:5], v[252:253]
	s_and_b64 vcc, exec, vcc
	s_cbranch_vccnz .LBB0_290
	s_ashr_i32 s0, s4, 31
	s_lshr_b32 s0, s0, 29
	s_add_i32 s0, s4, s0
	s_ashr_i32 s1, s0, 3
	s_and_b32 s0, s0, -8
	s_sub_i32 s0, s4, s0
	s_cmp_lt_i32 s0, 0
	s_cselect_b32 s8, s17, 0xc0
	s_mul_i32 s0, s0, s8
	s_add_i32 s0, s0, s1
	s_mul_hi_i32 s1, s0, 0x2aaaaaab
	s_lshr_b32 s8, s1, 31
	s_ashr_i32 s1, s1, 4
	s_add_i32 s1, s1, s8
	s_mul_i32 s8, s1, 0x60
	s_lshl_b32 s1, s1, 3
	s_sub_i32 s0, s0, s8
	s_sub_i32 s8, 0x80, s1
	s_min_i32 s8, s8, 8
	s_abs_i32 s8, s8
	s_sub_i32 s10, 0, s8
	s_ashr_i32 s9, s0, 31
	s_abs_i32 s0, s0
	s_nop 0
	s_mov_b32 s11, 0x1fffffc0
	s_mul_i32 s10, s10, s11
	s_mul_hi_u32 s10, s11, s10
	s_add_i32 s11, s11, s10
	s_mul_hi_u32 s10, s0, s11
	s_mul_i32 s10, s10, s8
	s_sub_i32 s0, s0, s10
	s_sub_i32 s10, s0, s8
	s_cmp_ge_u32 s0, s8
	s_cselect_b32 s0, s10, s0
	s_sub_i32 s10, s0, s8
	s_cmp_ge_u32 s0, s8
	s_cselect_b32 s0, s10, s0
	s_xor_b32 s0, s0, s9
	s_sub_i32 s0, s0, s9
	s_add_i32 s1, s1, s0
	v_lshl_add_u32 v4, s1, 8, v1
	v_readlane_b32 s0, v254, 63
	v_ashrrev_i32_e32 v5, 31, v4
	v_readlane_b32 s1, v255, 0
	s_add_u32 s4, s4, s88
	s_addc_u32 s5, s5, s7
	v_lshl_add_u64 v[4:5], v[4:5], 4, s[0:1]
	global_load_dwordx4 v[116:119], v[4:5], off
	v_cmp_gt_i64_e32 vcc, s[4:5], v[252:253]
	s_and_b64 vcc, exec, vcc
	s_cbranch_vccnz .LBB0_290
	s_ashr_i32 s0, s4, 31
	s_lshr_b32 s0, s0, 29
	s_add_i32 s0, s4, s0
	s_ashr_i32 s1, s0, 3
	s_and_b32 s0, s0, -8
	s_sub_i32 s0, s4, s0
	s_cmp_lt_i32 s0, 0
	s_cselect_b32 s8, s17, 0xc0
	s_mul_i32 s0, s0, s8
	s_add_i32 s0, s0, s1
	s_mul_hi_i32 s1, s0, 0x2aaaaaab
	s_lshr_b32 s8, s1, 31
	s_ashr_i32 s1, s1, 4
	s_add_i32 s1, s1, s8
	s_mul_i32 s8, s1, 0x60
	s_lshl_b32 s1, s1, 3
	s_sub_i32 s0, s0, s8
	s_sub_i32 s8, 0x80, s1
	s_min_i32 s8, s8, 8
	s_abs_i32 s8, s8
	s_sub_i32 s10, 0, s8
	s_ashr_i32 s9, s0, 31
	s_abs_i32 s0, s0
	s_nop 0
	s_mov_b32 s11, 0x1fffffc0
	s_mul_i32 s10, s10, s11
	s_mul_hi_u32 s10, s11, s10
	s_add_i32 s11, s11, s10
	s_mul_hi_u32 s10, s0, s11
	s_mul_i32 s10, s10, s8
	s_sub_i32 s0, s0, s10
	s_sub_i32 s10, s0, s8
	s_cmp_ge_u32 s0, s8
	s_cselect_b32 s0, s10, s0
	s_sub_i32 s10, s0, s8
	s_cmp_ge_u32 s0, s8
	s_cselect_b32 s0, s10, s0
	s_xor_b32 s0, s0, s9
	s_sub_i32 s0, s0, s9
	s_add_i32 s1, s1, s0
	v_lshl_add_u32 v4, s1, 8, v1
	v_readlane_b32 s0, v254, 63
	v_ashrrev_i32_e32 v5, 31, v4
	v_readlane_b32 s1, v255, 0
	s_add_u32 s4, s4, s88
	s_addc_u32 s5, s5, s7
	v_lshl_add_u64 v[4:5], v[4:5], 4, s[0:1]
	global_load_dwordx4 v[120:123], v[4:5], off
	v_cmp_gt_i64_e32 vcc, s[4:5], v[252:253]
	s_and_b64 vcc, exec, vcc
	s_cbranch_vccnz .LBB0_290
	s_ashr_i32 s0, s4, 31
	s_lshr_b32 s0, s0, 29
	s_add_i32 s0, s4, s0
	s_ashr_i32 s1, s0, 3
	s_and_b32 s0, s0, -8
	s_sub_i32 s0, s4, s0
	s_cmp_lt_i32 s0, 0
	s_cselect_b32 s4, s17, 0xc0
	s_mul_i32 s0, s0, s4
	s_add_i32 s0, s0, s1
	s_mul_hi_i32 s1, s0, 0x2aaaaaab
	s_lshr_b32 s4, s1, 31
	s_ashr_i32 s1, s1, 4
	s_add_i32 s1, s1, s4
	s_lshl_b32 s4, s1, 3
	s_sub_i32 s5, 0x80, s4
	s_min_i32 s5, s5, 8
	s_abs_i32 s5, s5
	s_sub_i32 s7, 0, s5
	s_mulk_i32 s1, 0x60
	s_sub_i32 s0, s0, s1
	s_ashr_i32 s1, s0, 31
	s_abs_i32 s0, s0
	s_mov_b32 s8, 0x1fffffc0
	s_mul_i32 s7, s7, s8
	s_mul_hi_u32 s7, s8, s7
	s_add_i32 s8, s8, s7
	s_mul_hi_u32 s7, s0, s8
	s_mul_i32 s7, s7, s5
	s_sub_i32 s0, s0, s7
	s_sub_i32 s7, s0, s5
	s_cmp_ge_u32 s0, s5
	s_cselect_b32 s0, s7, s0
	s_sub_i32 s7, s0, s5
	s_cmp_ge_u32 s0, s5
	s_cselect_b32 s0, s7, s0
	s_xor_b32 s0, s0, s1
	s_sub_i32 s0, s0, s1
	s_add_i32 s4, s4, s0
	v_lshl_add_u32 v4, s4, 8, v1
	v_readlane_b32 s0, v254, 63
	v_ashrrev_i32_e32 v5, 31, v4
	v_readlane_b32 s1, v255, 0
	s_nop 1
	v_lshl_add_u64 v[4:5], v[4:5], 4, s[0:1]
	global_load_dwordx4 v[124:127], v[4:5], off

;     __host__ __device__ bool next(int i, Unit& u) const {
;         const long L = (long)i * G + c; if (L >= nwg) return false;
;         int wgid = (int)L; { const int q = nwg / NXCD, r = nwg % NXCD, xcd = wgid % NXCD, off = wgid / NXCD; wgid = (xcd < r ? xcd * (q + 1) : r * (q + 1) + (xcd - r) * q) + off; }
;         const int nig = WGM * nN, gid = wgid / nig, fm = gid * WGM, gsz = (nM - fm) < WGM ? (nM - fm) : WGM;
;         u.pm = fm + ((wgid % nig) % gsz); u.pn = (wgid % nig) / gsz; u.idx = i; return true;
; template <class Epi, class Sched, bool ALIGN_EPI = false, bool SP2 = false>
; __device__ __forceinline__ void gemm_phase(PG8_LAS unsigned char* lds, const Gemm g, const Sched& S, const Epi& E, const int tid) {
;     ...
;         const bool has_next = S.next(ui + 1, nxt);
;         const char* nA = has_next ? (const char*)g.A + (size_t)nxt.pm * tstep : cA; const char* nB = has_next ? (const char*)g.Bt + (size_t)nxt.pn * tstep : cB;
.LBB0_296:
	s_add_i32 s60, s60, 1
	s_mul_i32 s2, s60, s57
	s_mul_hi_u32 s3, s60, s88
	s_add_i32 s3, s3, s2
	s_mul_i32 s2, s60, s88
	s_add_u32 s12, s2, s90
	s_addc_u32 s13, s3, s40
	v_mov_b64_e32 v[4:5], 0x600
	v_cmp_gt_i64_e32 vcc, s[12:13], v[252:253]
	v_cmp_lt_i64_e64 s[2:3], s[12:13], v[4:5]
	s_cbranch_vccnz .LBB0_298
	s_ashr_i32 s8, s12, 31
	s_lshr_b32 s8, s8, 29
	s_add_i32 s8, s12, s8
	s_ashr_i32 s9, s8, 3
	s_and_b32 s8, s8, -8
	s_sub_i32 s8, s12, s8
	s_cmp_lt_i32 s8, 0
	s_cselect_b32 s10, s17, 0xc0
	s_mul_i32 s8, s8, s10
	s_add_i32 s8, s8, s9
	s_mul_hi_i32 s9, s8, 0x2aaaaaab
	s_lshr_b32 s10, s9, 31
	s_ashr_i32 s9, s9, 4
	s_add_i32 s9, s9, s10
	s_lshl_b32 s10, s9, 3
	s_sub_i32 s11, 0x80, s10
	s_min_i32 s11, s11, 8
	s_abs_i32 s12, s11
	s_sub_i32 s14, 0, s12
	s_mulk_i32 s9, 0x60
	s_sub_i32 s9, s8, s9
	s_abs_i32 s8, s9
	s_xor_b32 s13, s9, s11
	s_ashr_i32 s13, s13, 31
	s_mov_b32 s62, s60
	s_mov_b32 s15, 0x1fffffc0
	s_mul_i32 s14, s14, s15
	s_mul_hi_u32 s14, s15, s14
	s_add_i32 s15, s15, s14
	s_mul_hi_u32 s14, s8, s15
	s_mul_i32 s15, s14, s12
	s_sub_i32 s8, s8, s15
	s_add_i32 s36, s14, 1
	s_sub_i32 s15, s8, s12
	s_cmp_ge_u32 s8, s12
	s_cselect_b32 s14, s36, s14
	s_cselect_b32 s8, s15, s8
	s_add_i32 s15, s14, 1
	s_cmp_ge_u32 s8, s12
	s_cselect_b32 s8, s15, s14
	s_xor_b32 s8, s8, s13
	s_sub_i32 s8, s8, s13
	s_mul_i32 s11, s8, s11
	s_sub_i32 s9, s9, s11
	s_add_i32 s10, s10, s9

;     __host__ __device__ bool next(int i, Unit& u) const {
;         const long L = (long)i * G + c; if (L >= nwg) return false;
;         int wgid = (int)L; { const int q = nwg / NXCD, r = nwg % NXCD, xcd = wgid % NXCD, off = wgid / NXCD; wgid = (xcd < r ? xcd * (q + 1) : r * (q + 1) + (xcd - r) * q) + off; }
;         const int nig = WGM * nN, gid = wgid / nig, fm = gid * WGM, gsz = (nM - fm) < WGM ? (nM - fm) : WGM;
;         u.pm = fm + ((wgid % nig) % gsz); u.pn = (wgid % nig) / gsz; u.idx = i; return true;
; template <class Sched> __device__ __forceinline__ void stage_scales(PG8_LAS unsigned char* lds, const Sched& S, const float* rs, bool cols, int ldil, int tid) {
;     ...
;         for (int i = 0; i < 16 && S.next(i, u); ++i) { const f32x4 a = *(const f32x4*)(rs + 4 * (size_t)(cols ? u.pn * BM + tm : u.pm * BM + tid));
;             tab[i * 256 + tid] = __builtin_amdgcn_rsqf(((a[0] + a[1]) + (a[2] + a[3])) * (1.0f / 1024.0f) + eps); } }
.LBB0_314:
	s_ashr_i32 s6, s8, 3
	s_add_i32 s6, s9, s6
	s_ashr_i32 s7, s6, 31
	s_lshr_b32 s7, s7, 25
	s_add_i32 s7, s6, s7
	s_ashr_i32 s8, s7, 7
	s_and_b32 s7, s7, 0xffffff80
	s_sub_i32 s6, s6, s7
	s_lshl_b32 s7, s8, 3
	s_sub_i32 s8, 0x80, s7
	s_min_i32 s8, s8, 8
	s_abs_i32 s8, s8
	s_sub_i32 s14, 0, s8
	s_ashr_i32 s9, s6, 31
	s_abs_i32 s6, s6
	s_addk_i32 s13, 0x800
	v_add_u32_e32 v2, 0x24400, v2
	s_mov_b32 s15, 0x1fffffc0
	s_mul_i32 s14, s14, s15
	s_mul_hi_u32 s14, s15, s14
	s_add_i32 s15, s15, s14
	s_mul_hi_u32 s14, s6, s15
	s_mul_i32 s14, s14, s8
	s_sub_i32 s6, s6, s14
	s_sub_i32 s14, s6, s8
	s_cmp_ge_u32 s6, s8
	s_cselect_b32 s6, s14, s6
	s_sub_i32 s14, s6, s8
	s_cmp_ge_u32 s6, s8
	s_cselect_b32 s6, s14, s6
	s_xor_b32 s6, s6, s9
	s_sub_i32 s6, s6, s9
	s_add_i32 s7, s7, s6
	v_lshl_add_u32 v4, s7, 8, v0
	v_readlane_b32 s6, v254, 63
	v_ashrrev_i32_e32 v5, 31, v4
	v_readlane_b32 s7, v255, 0
	s_cmp_eq_u32 s13, 0
	s_cselect_b64 s[8:9], -1, 0
	v_lshl_add_u64 v[4:5], v[4:5], 4, s[6:7]
	global_load_dwordx4 v[4:7], v[4:5], off
	s_waitcnt vmcnt(0)
	v_mov_b32_e32 v8, v5
	v_mov_b32_e32 v9, v6
	v_mov_b32_e32 v5, v7
	v_pk_add_f32 v[4:5], v[8:9], v[4:5]
	s_nop 0
	v_add_f32_e32 v4, v4, v5
	v_mov_b32_e32 v5, s10
	v_fmamk_f32 v4, v4, 0x3a800000, v5
	v_rsq_f32_e32 v4, v4
	ds_write_b32 v2, v4

;     __host__ __device__ bool next(int i, Unit& u) const {
;         const long L = (long)i * G + c; if (L >= nwg) return false;
;         int wgid = (int)L; { const int q = nwg / NXCD, r = nwg % NXCD, xcd = wgid % NXCD, off = wgid / NXCD; wgid = (xcd < r ? xcd * (q + 1) : r * (q + 1) + (xcd - r) * q) + off; }
;         const int nig = WGM * nN, gid = wgid / nig, fm = gid * WGM, gsz = (nM - fm) < WGM ? (nM - fm) : WGM;
;         u.pm = fm + ((wgid % nig) % gsz); u.pn = (wgid % nig) / gsz; u.idx = i; return true;
; template <class Sched> __device__ __forceinline__ void stage_scales(PG8_LAS unsigned char* lds, const Sched& S, const float* rs, bool cols, int ldil, int tid) {
;     ...
;         for (int i = 0; i < 16 && S.next(i, u); ++i) { const f32x4 a = *(const f32x4*)(rs + 4 * (size_t)(cols ? u.pn * BM + tm : u.pm * BM + tid));
;             tab[i * 256 + tid] = __builtin_amdgcn_rsqf(((a[0] + a[1]) + (a[2] + a[3])) * (1.0f / 1024.0f) + eps); } }
.LBB0_321:
	s_ashr_i32 s4, s8, 3
	s_add_i32 s4, s14, s4
	s_ashr_i32 s5, s4, 31
	s_lshr_b32 s5, s5, 25
	s_add_i32 s5, s4, s5
	s_ashr_i32 s8, s5, 7
	s_and_b32 s5, s5, 0xffffff80
	s_sub_i32 s4, s4, s5
	s_lshl_b32 s5, s8, 3
	s_sub_i32 s8, 0x80, s5
	s_min_i32 s8, s8, 8
	s_abs_i32 s8, s8
	s_sub_i32 s14, 0, s8
	s_ashr_i32 s9, s4, 31
	s_abs_i32 s4, s4
	s_nop 0
	s_mov_b32 s15, 0x1fffffc0
	s_mul_i32 s14, s14, s15
	s_mul_hi_u32 s14, s15, s14
	s_add_i32 s15, s15, s14
	s_mul_hi_u32 s14, s4, s15
	s_mul_i32 s14, s14, s8
	s_sub_i32 s4, s4, s14
	s_sub_i32 s14, s4, s8
	s_cmp_ge_u32 s4, s8
	s_cselect_b32 s4, s14, s4
	s_sub_i32 s14, s4, s8
	s_cmp_ge_u32 s4, s8
	s_cselect_b32 s4, s14, s4
	s_xor_b32 s4, s4, s9
	s_sub_i32 s4, s4, s9
	s_add_i32 s5, s5, s4
	v_lshl_add_u32 v4, s5, 8, v0
	v_readlane_b32 s4, v254, 63
	v_ashrrev_i32_e32 v5, 31, v4
	v_readlane_b32 s5, v255, 0
	s_nop 1
	v_lshl_add_u64 v[4:5], v[4:5], 4, s[4:5]
	global_load_dwordx4 v[4:7], v[4:5], off
	s_add_u32 s4, s6, s2
	s_addc_u32 s5, s7, s3
	s_add_u32 s8, s11, s4
	s_addc_u32 s9, s12, s5
	v_cmp_gt_i64_e32 vcc, s[8:9], v[206:207]
	s_mov_b64 s[8:9], -1
	s_and_b64 vcc, exec, vcc
	s_waitcnt vmcnt(0)
	v_mov_b32_e32 v8, v5
	v_mov_b32_e32 v9, v6
	v_mov_b32_e32 v5, v7
	v_pk_add_f32 v[4:5], v[8:9], v[4:5]
	s_nop 0
	v_add_f32_e32 v2, v4, v5
	v_mov_b32_e32 v4, s10
	v_fmamk_f32 v2, v2, 0x3a800000, v4
	v_rsq_f32_e32 v4, v2
	v_add_u32_e32 v2, s13, v1
	v_add_u32_e32 v5, 0x24000, v2
	ds_write_b32 v5, v4
	s_cbranch_vccnz .LBB0_315
	s_add_i32 s6, s88, s6
	s_ashr_i32 s7, s6, 31
	s_lshr_b32 s7, s7, 29
	s_add_i32 s8, s6, s7
	s_and_b32 s7, s8, -8
	s_sub_i32 s14, s6, s7
	s_cmp_lt_i32 s14, 0
	s_mov_b64 s[6:7], -1
	s_cbranch_scc1 .LBB0_324
	s_lshl_b32 s9, s14, 8
	s_mov_b64 s[6:7], 0

;     __host__ __device__ bool next(int i, Unit& u) const {
;         const long L = (long)i * G + c; if (L >= nwg) return false;
;         int wgid = (int)L; { const int q = nwg / NXCD, r = nwg % NXCD, xcd = wgid % NXCD, off = wgid / NXCD; wgid = (xcd < r ? xcd * (q + 1) : r * (q + 1) + (xcd - r) * q) + off; }
;         const int nig = WGM * nN, gid = wgid / nig, fm = gid * WGM, gsz = (nM - fm) < WGM ? (nM - fm) : WGM;
;         u.pm = fm + ((wgid % nig) % gsz); u.pn = (wgid % nig) / gsz; u.idx = i; return true;
; template <class Epi, class Sched, bool ALIGN_EPI = false, bool SP2 = false>
; __device__ __forceinline__ void gemm_phase(PG8_LAS unsigned char* lds, const Gemm g, const Sched& S, const Epi& E, const int tid) {
;     ...
;         const bool has_next = S.next(ui + 1, nxt);
;         const char* nA = has_next ? (const char*)g.A + (size_t)nxt.pm * tstep : cA; const char* nB = has_next ? (const char*)g.Bt + (size_t)nxt.pn * tstep : cB;
.LBB0_341:
	s_ashr_i32 s8, s10, 3
	s_add_i32 s8, s12, s8
	s_ashr_i32 s9, s8, 31
	s_lshr_b32 s9, s9, 25
	s_add_i32 s9, s8, s9
	s_ashr_i32 s10, s9, 7
	s_lshl_b32 s10, s10, 3
	s_sub_i32 s11, 0x80, s10
	s_min_i32 s11, s11, 8
	s_abs_i32 s12, s11
	s_sub_i32 s14, 0, s12
	s_and_b32 s9, s9, 0xffffff80
	s_sub_i32 s9, s8, s9
	s_abs_i32 s8, s9
	s_xor_b32 s13, s9, s11
	s_ashr_i32 s13, s13, 31
	s_mov_b32 s80, s79
	s_mov_b32 s15, 0x1fffffc0
	s_mul_i32 s14, s14, s15
	s_mul_hi_u32 s14, s15, s14
	s_add_i32 s15, s15, s14
	s_mul_hi_u32 s14, s8, s15
	s_mul_i32 s15, s14, s12
	s_sub_i32 s8, s8, s15
	s_add_i32 s36, s14, 1
	s_sub_i32 s15, s8, s12
	s_cmp_ge_u32 s8, s12
	s_cselect_b32 s14, s36, s14
	s_cselect_b32 s8, s15, s8
	s_add_i32 s15, s14, 1
	s_cmp_ge_u32 s8, s12
	s_cselect_b32 s8, s15, s14
	s_xor_b32 s8, s8, s13
	s_sub_i32 s8, s8, s13
	s_mul_i32 s11, s8, s11
	s_sub_i32 s9, s9, s11
	s_add_i32 s10, s10, s9

;     __host__ __device__ bool next(int i, Unit& u) const {
;         const long L = (long)i * G + c; if (L >= nwg) return false;
;         int wgid = (int)L; { const int q = nwg / NXCD, r = nwg % NXCD, xcd = wgid % NXCD, off = wgid / NXCD; wgid = (xcd < r ? xcd * (q + 1) : r * (q + 1) + (xcd - r) * q) + off; }
;         const int nig = WGM * nN, gid = wgid / nig, fm = gid * WGM, gsz = (nM - fm) < WGM ? (nM - fm) : WGM;
;         u.pm = fm + ((wgid % nig) % gsz); u.pn = (wgid % nig) / gsz; u.idx = i; return true;
; template <class Sched> __device__ __forceinline__ void stage_scales(PG8_LAS unsigned char* lds, const Sched& S, const float* rs, bool cols, int ldil, int tid) {
;     ...
;     if (tid < 256) { const int lper = 8 - ldil, c = tid, tm = ((c & ((1 << lper) - 1)) << ldil) + (c >> lper);
;         float eps = 1e-6f; asm volatile("" : "+s"(eps));
;         for (int i = 0; i < 16 && S.next(i, u); ++i) { const f32x4 a = *(const f32x4*)(rs + 4 * (size_t)(cols ? u.pn * BM + tm : u.pm * BM + tid));
;             tab[i * 256 + tid] = __builtin_amdgcn_rsqf(((a[0] + a[1]) + (a[2] + a[3])) * (1.0f / 1024.0f) + eps); } }
.LBB0_698:
	v_readlane_b32 s0, v255, 1
	v_readlane_b32 s1, v255, 2
	s_and_b64 vcc, exec, s[0:1]
	s_cbranch_vccz .LBB0_797
	v_readlane_b32 s0, v254, 59
	s_cmp_gt_i32 s0, 0
	s_mov_b64 s[0:1], -1
	s_cbranch_scc0 .LBB0_735
	v_mbcnt_lo_u32_b32 v16, -1, 0
	v_mbcnt_hi_u32_b32 v16, -1, v16
	s_movk_i32 s0, 0x100
	v_add_u32_e32 v1, s30, v16
	v_cmp_gt_i32_e32 vcc, s0, v1
	s_and_saveexec_b64 s[0:1], vcc
	s_cbranch_execz .LBB0_718
	s_mov_b32 s4, 0x358637bd
	s_cmpk_gt_i32 s90, 0xaff
	s_cbranch_scc1 .LBB0_718
	s_ashr_i32 s3, s90, 31
	s_lshr_b32 s2, s3, 29
	s_add_i32 s2, s90, s2
	s_ashr_i32 s6, s2, 3
	s_and_b32 s2, s2, -8
	s_ashr_i32 s5, s88, 31
	s_sub_i32 s2, s90, s2
	s_cmp_lt_i32 s2, 0
	s_movk_i32 s7, 0x161
	s_cselect_b32 s7, s7, 0x160
	s_mul_i32 s2, s2, s7
	s_add_i32 s2, s2, s6
	s_mul_hi_i32 s6, s2, 0x2e8ba2e9
	s_lshr_b32 s7, s6, 31
	s_ashr_i32 s6, s6, 5
	s_add_i32 s6, s6, s7
	s_lshl_b32 s7, s6, 3
	s_sub_i32 s8, 0x80, s7
	s_min_i32 s8, s8, 8
	s_abs_i32 s8, s8
	s_sub_i32 s9, 0, s8
	s_mulk_i32 s6, 0xb0
	s_sub_i32 s2, s2, s6
	s_ashr_i32 s6, s2, 31
	s_abs_i32 s2, s2
	v_mov_b32_e32 v2, s4
	s_mov_b32 s10, 0x1fffffc0
	s_mul_i32 s9, s9, s10
	s_mul_hi_u32 s9, s10, s9
	s_add_i32 s10, s10, s9
	s_mul_hi_u32 s9, s2, s10
	s_mul_i32 s9, s9, s8
	s_sub_i32 s2, s2, s9
	s_sub_i32 s9, s2, s8
	s_cmp_ge_u32 s2, s8
	s_cselect_b32 s2, s9, s2
	s_sub_i32 s9, s2, s8
	s_cmp_ge_u32 s2, s8
	s_cselect_b32 s2, s9, s2
	s_xor_b32 s2, s2, s6
	s_sub_i32 s2, s2, s6
	s_add_i32 s7, s7, s2
	v_lshl_add_u32 v4, s7, 8, v1
	v_readlane_b32 s6, v254, 63
	s_waitcnt lgkmcnt(0)
	v_ashrrev_i32_e32 v5, 31, v4
	v_readlane_b32 s7, v255, 0
	s_add_u32 s2, s88, s90
	s_addc_u32 s3, s5, s3
	v_lshl_add_u64 v[4:5], v[4:5], 4, s[6:7]
	global_load_dwordx4 v[64:67], v[4:5], off
	v_lshl_add_u32 v0, v1, 2, 0
	v_add_u32_e32 v0, 0x20000, v0
	v_mov_b64_e32 v[4:5], 0xaff
	v_cmp_gt_i64_e32 vcc, s[2:3], v[4:5]
	s_cbranch_vccnz .LBB0_718
	s_ashr_i32 s6, s2, 31
	s_lshr_b32 s6, s6, 29
	s_add_i32 s6, s2, s6
	s_ashr_i32 s7, s6, 3
	s_and_b32 s6, s6, -8
	s_sub_i32 s6, s2, s6
	s_cmp_lt_i32 s6, 0
	s_movk_i32 s8, 0x161
	s_cselect_b32 s8, s8, 0x160
	s_mul_i32 s6, s6, s8
	s_add_i32 s6, s6, s7
	s_mul_hi_i32 s7, s6, 0x2e8ba2e9
	s_lshr_b32 s8, s7, 31
	s_ashr_i32 s7, s7, 5
	s_add_i32 s7, s7, s8
	s_lshl_b32 s8, s7, 3
	s_sub_i32 s9, 0x80, s8
	s_min_i32 s9, s9, 8
	s_abs_i32 s9, s9
	s_sub_i32 s10, 0, s9
	s_mulk_i32 s7, 0xb0
	s_sub_i32 s6, s6, s7
	s_ashr_i32 s7, s6, 31
	s_abs_i32 s6, s6
	s_mov_b32 s11, 0x1fffffc0
	s_mul_i32 s10, s10, s11
	s_mul_hi_u32 s10, s11, s10
	s_add_i32 s11, s11, s10
	s_mul_hi_u32 s10, s6, s11
	s_mul_i32 s10, s10, s9
	s_sub_i32 s6, s6, s10
	s_sub_i32 s10, s6, s9
	s_cmp_ge_u32 s6, s9
	s_cselect_b32 s6, s10, s6
	s_sub_i32 s10, s6, s9
	s_cmp_ge_u32 s6, s9
	s_cselect_b32 s6, s10, s6
	s_xor_b32 s6, s6, s7
	s_sub_i32 s6, s6, s7
	s_add_i32 s8, s8, s6
	v_lshl_add_u32 v4, s8, 8, v1
	v_readlane_b32 s6, v254, 63
	v_ashrrev_i32_e32 v5, 31, v4
	v_readlane_b32 s7, v255, 0
	v_mov_b32_e32 v2, s4
	s_add_u32 s2, s2, s88
	v_lshl_add_u64 v[4:5], v[4:5], 4, s[6:7]
	global_load_dwordx4 v[68:71], v[4:5], off
	s_addc_u32 s3, s3, s5
	v_mov_b64_e32 v[4:5], 0xaff
	v_cmp_gt_i64_e32 vcc, s[2:3], v[4:5]
	s_cbranch_vccnz .LBB0_718
	s_ashr_i32 s6, s2, 31
	s_lshr_b32 s6, s6, 29
	s_add_i32 s6, s2, s6
	s_ashr_i32 s7, s6, 3
	s_and_b32 s6, s6, -8
	s_sub_i32 s6, s2, s6
	s_cmp_lt_i32 s6, 0
	s_movk_i32 s8, 0x161
	s_cselect_b32 s8, s8, 0x160
	s_mul_i32 s6, s6, s8
	s_add_i32 s6, s6, s7
	s_mul_hi_i32 s7, s6, 0x2e8ba2e9
	s_lshr_b32 s8, s7, 31
	s_ashr_i32 s7, s7, 5
	s_add_i32 s7, s7, s8
	s_lshl_b32 s8, s7, 3
	s_sub_i32 s9, 0x80, s8
	s_min_i32 s9, s9, 8
	s_abs_i32 s9, s9
	s_sub_i32 s10, 0, s9
	s_mulk_i32 s7, 0xb0
	s_sub_i32 s6, s6, s7
	s_ashr_i32 s7, s6, 31
	s_abs_i32 s6, s6
	s_mov_b32 s11, 0x1fffffc0
	s_mul_i32 s10, s10, s11
	s_mul_hi_u32 s10, s11, s10
	s_add_i32 s11, s11, s10
	s_mul_hi_u32 s10, s6, s11
	s_mul_i32 s10, s10, s9
	s_sub_i32 s6, s6, s10
	s_sub_i32 s10, s6, s9
	s_cmp_ge_u32 s6, s9
	s_cselect_b32 s6, s10, s6
	s_sub_i32 s10, s6, s9
	s_cmp_ge_u32 s6, s9
	s_cselect_b32 s6, s10, s6
	s_xor_b32 s6, s6, s7
	s_sub_i32 s6, s6, s7
	s_add_i32 s8, s8, s6
	v_lshl_add_u32 v4, s8, 8, v1
	v_readlane_b32 s6, v254, 63
	v_ashrrev_i32_e32 v5, 31, v4
	v_readlane_b32 s7, v255, 0
	v_mov_b32_e32 v2, s4
	s_add_u32 s2, s2, s88
	v_lshl_add_u64 v[4:5], v[4:5], 4, s[6:7]
	global_load_dwordx4 v[72:75], v[4:5], off
	s_addc_u32 s3, s3, s5
	v_mov_b64_e32 v[4:5], 0xaff
	v_cmp_gt_i64_e32 vcc, s[2:3], v[4:5]
	s_cbranch_vccnz .LBB0_718
	s_ashr_i32 s6, s2, 31
	s_lshr_b32 s6, s6, 29
	s_add_i32 s6, s2, s6
	s_ashr_i32 s7, s6, 3
	s_and_b32 s6, s6, -8
	s_sub_i32 s6, s2, s6
	s_cmp_lt_i32 s6, 0
	s_movk_i32 s8, 0x161
	s_cselect_b32 s8, s8, 0x160
	s_mul_i32 s6, s6, s8
	s_add_i32 s6, s6, s7
	s_mul_hi_i32 s7, s6, 0x2e8ba2e9
	s_lshr_b32 s8, s7, 31
	s_ashr_i32 s7, s7, 5
	s_add_i32 s7, s7, s8
	s_lshl_b32 s8, s7, 3
	s_sub_i32 s9, 0x80, s8
	s_min_i32 s9, s9, 8
	s_abs_i32 s9, s9
	s_sub_i32 s10, 0, s9
	s_mulk_i32 s7, 0xb0
	s_sub_i32 s6, s6, s7
	s_ashr_i32 s7, s6, 31
	s_abs_i32 s6, s6
	s_mov_b32 s11, 0x1fffffc0
	s_mul_i32 s10, s10, s11
	s_mul_hi_u32 s10, s11, s10
	s_add_i32 s11, s11, s10
	s_mul_hi_u32 s10, s6, s11
	s_mul_i32 s10, s10, s9
	s_sub_i32 s6, s6, s10
	s_sub_i32 s10, s6, s9
	s_cmp_ge_u32 s6, s9
	s_cselect_b32 s6, s10, s6
	s_sub_i32 s10, s6, s9
	s_cmp_ge_u32 s6, s9
	s_cselect_b32 s6, s10, s6
	s_xor_b32 s6, s6, s7
	s_sub_i32 s6, s6, s7
	s_add_i32 s8, s8, s6
	v_lshl_add_u32 v4, s8, 8, v1
	v_readlane_b32 s6, v254, 63
	v_ashrrev_i32_e32 v5, 31, v4
	v_readlane_b32 s7, v255, 0
	v_mov_b32_e32 v2, s4
	s_add_u32 s2, s2, s88
	v_lshl_add_u64 v[4:5], v[4:5], 4, s[6:7]
	global_load_dwordx4 v[76:79], v[4:5], off
	s_addc_u32 s3, s3, s5
	v_mov_b64_e32 v[4:5], 0xaff
	v_cmp_gt_i64_e32 vcc, s[2:3], v[4:5]
	s_cbranch_vccnz .LBB0_718
;     __host__ __device__ bool next(int i, Unit& u) const {
;         const long L = (long)i * G + c; if (L >= nwg) return false;
;         int wgid = (int)L; { const int q = nwg / NXCD, r = nwg % NXCD, xcd = wgid % NXCD, off = wgid / NXCD; wgid = (xcd < r ? xcd * (q + 1) : r * (q + 1) + (xcd - r) * q) + off; }
;         const int nig = WGM * nN, gid = wgid / nig, fm = gid * WGM, gsz = (nM - fm) < WGM ? (nM - fm) : WGM;
;         u.pm = fm + ((wgid % nig) % gsz); u.pn = (wgid % nig) / gsz; u.idx = i; return true;
; template <class Sched> __device__ __forceinline__ void stage_scales(PG8_LAS unsigned char* lds, const Sched& S, const float* rs, bool cols, int ldil, int tid) {
;     ...
;     if (tid < 256) { const int lper = 8 - ldil, c = tid, tm = ((c & ((1 << lper) - 1)) << ldil) + (c >> lper);
;         float eps = 1e-6f; asm volatile("" : "+s"(eps));
;         for (int i = 0; i < 16 && S.next(i, u); ++i) { const f32x4 a = *(const f32x4*)(rs + 4 * (size_t)(cols ? u.pn * BM + tm : u.pm * BM + tid));
;             tab[i * 256 + tid] = __builtin_amdgcn_rsqf(((a[0] + a[1]) + (a[2] + a[3])) * (1.0f / 1024.0f) + eps); } }
	s_ashr_i32 s6, s2, 31
	s_lshr_b32 s6, s6, 29
	s_add_i32 s6, s2, s6
	s_ashr_i32 s7, s6, 3
	s_and_b32 s6, s6, -8
	s_sub_i32 s6, s2, s6
	s_cmp_lt_i32 s6, 0
	s_movk_i32 s8, 0x161
	s_cselect_b32 s8, s8, 0x160
	s_mul_i32 s6, s6, s8
	s_add_i32 s6, s6, s7
	s_mul_hi_i32 s7, s6, 0x2e8ba2e9
	s_lshr_b32 s8, s7, 31
	s_ashr_i32 s7, s7, 5
	s_add_i32 s7, s7, s8
	s_lshl_b32 s8, s7, 3
	s_sub_i32 s9, 0x80, s8
	s_min_i32 s9, s9, 8
	s_abs_i32 s9, s9
	s_sub_i32 s10, 0, s9
	s_mulk_i32 s7, 0xb0
	s_sub_i32 s6, s6, s7
	s_ashr_i32 s7, s6, 31
	s_abs_i32 s6, s6
	s_mov_b32 s11, 0x1fffffc0
	s_mul_i32 s10, s10, s11
	s_mul_hi_u32 s10, s11, s10
	s_add_i32 s11, s11, s10
	s_mul_hi_u32 s10, s6, s11
	s_mul_i32 s10, s10, s9
	s_sub_i32 s6, s6, s10
	s_sub_i32 s10, s6, s9
	s_cmp_ge_u32 s6, s9
	s_cselect_b32 s6, s10, s6
	s_sub_i32 s10, s6, s9
	s_cmp_ge_u32 s6, s9
	s_cselect_b32 s6, s10, s6
	s_xor_b32 s6, s6, s7
	s_sub_i32 s6, s6, s7
	s_add_i32 s8, s8, s6
	v_lshl_add_u32 v4, s8, 8, v1
	v_readlane_b32 s6, v254, 63
	v_ashrrev_i32_e32 v5, 31, v4
	v_readlane_b32 s7, v255, 0
	v_mov_b32_e32 v2, s4
	s_add_u32 s2, s2, s88
	v_lshl_add_u64 v[4:5], v[4:5], 4, s[6:7]
	global_load_dwordx4 v[80:83], v[4:5], off
	s_addc_u32 s3, s3, s5
	v_mov_b64_e32 v[4:5], 0xaff
	v_cmp_gt_i64_e32 vcc, s[2:3], v[4:5]
	s_cbranch_vccnz .LBB0_718
	s_ashr_i32 s6, s2, 31
	s_lshr_b32 s6, s6, 29
	s_add_i32 s6, s2, s6
	s_ashr_i32 s7, s6, 3
	s_and_b32 s6, s6, -8
	s_sub_i32 s6, s2, s6
	s_cmp_lt_i32 s6, 0
	s_movk_i32 s8, 0x161
	s_cselect_b32 s8, s8, 0x160
	s_mul_i32 s6, s6, s8
	s_add_i32 s6, s6, s7
	s_mul_hi_i32 s7, s6, 0x2e8ba2e9
	s_lshr_b32 s8, s7, 31
	s_ashr_i32 s7, s7, 5
	s_add_i32 s7, s7, s8
	s_lshl_b32 s8, s7, 3
	s_sub_i32 s9, 0x80, s8
	s_min_i32 s9, s9, 8
	s_abs_i32 s9, s9
	s_sub_i32 s10, 0, s9
	s_mulk_i32 s7, 0xb0
	s_sub_i32 s6, s6, s7
	s_ashr_i32 s7, s6, 31
	s_abs_i32 s6, s6
	s_mov_b32 s11, 0x1fffffc0
	s_mul_i32 s10, s10, s11
	s_mul_hi_u32 s10, s11, s10
	s_add_i32 s11, s11, s10
	s_mul_hi_u32 s10, s6, s11
	s_mul_i32 s10, s10, s9
	s_sub_i32 s6, s6, s10
	s_sub_i32 s10, s6, s9
	s_cmp_ge_u32 s6, s9
	s_cselect_b32 s6, s10, s6
	s_sub_i32 s10, s6, s9
	s_cmp_ge_u32 s6, s9
	s_cselect_b32 s6, s10, s6
	s_xor_b32 s6, s6, s7
	s_sub_i32 s6, s6, s7
	s_add_i32 s8, s8, s6
	v_lshl_add_u32 v4, s8, 8, v1
	v_readlane_b32 s6, v254, 63
	v_ashrrev_i32_e32 v5, 31, v4
	v_readlane_b32 s7, v255, 0
	v_mov_b32_e32 v2, s4
	s_add_u32 s2, s2, s88
	v_lshl_add_u64 v[4:5], v[4:5], 4, s[6:7]
	global_load_dwordx4 v[84:87], v[4:5], off
	s_addc_u32 s3, s3, s5
	v_mov_b64_e32 v[4:5], 0xaff
	v_cmp_gt_i64_e32 vcc, s[2:3], v[4:5]
	s_cbranch_vccnz .LBB0_718
	s_ashr_i32 s6, s2, 31
	s_lshr_b32 s6, s6, 29
	s_add_i32 s6, s2, s6
	s_ashr_i32 s7, s6, 3
	s_and_b32 s6, s6, -8
	s_sub_i32 s6, s2, s6
	s_cmp_lt_i32 s6, 0
	s_movk_i32 s8, 0x161
	s_cselect_b32 s8, s8, 0x160
	s_mul_i32 s6, s6, s8
	s_add_i32 s6, s6, s7
	s_mul_hi_i32 s7, s6, 0x2e8ba2e9
	s_lshr_b32 s8, s7, 31
	s_ashr_i32 s7, s7, 5
	s_add_i32 s7, s7, s8
	s_lshl_b32 s8, s7, 3
	s_sub_i32 s9, 0x80, s8
	s_min_i32 s9, s9, 8
	s_abs_i32 s9, s9
	s_sub_i32 s10, 0, s9
	s_mulk_i32 s7, 0xb0
	s_sub_i32 s6, s6, s7
	s_ashr_i32 s7, s6, 31
	s_abs_i32 s6, s6
	s_mov_b32 s11, 0x1fffffc0
	s_mul_i32 s10, s10, s11
	s_mul_hi_u32 s10, s11, s10
	s_add_i32 s11, s11, s10
	s_mul_hi_u32 s10, s6, s11
	s_mul_i32 s10, s10, s9
	s_sub_i32 s6, s6, s10
	s_sub_i32 s10, s6, s9
	s_cmp_ge_u32 s6, s9
	s_cselect_b32 s6, s10, s6
	s_sub_i32 s10, s6, s9
	s_cmp_ge_u32 s6, s9
	s_cselect_b32 s6, s10, s6
	s_xor_b32 s6, s6, s7
	s_sub_i32 s6, s6, s7
	s_add_i32 s8, s8, s6
	v_lshl_add_u32 v4, s8, 8, v1
	v_readlane_b32 s6, v254, 63
	v_ashrrev_i32_e32 v5, 31, v4
	v_readlane_b32 s7, v255, 0
	v_mov_b32_e32 v2, s4
	s_add_u32 s2, s2, s88
	v_lshl_add_u64 v[4:5], v[4:5], 4, s[6:7]
	global_load_dwordx4 v[88:91], v[4:5], off
	s_addc_u32 s3, s3, s5
	v_mov_b64_e32 v[4:5], 0xaff
	v_cmp_gt_i64_e32 vcc, s[2:3], v[4:5]
	s_cbranch_vccnz .LBB0_718
	s_ashr_i32 s6, s2, 31
	s_lshr_b32 s6, s6, 29
	s_add_i32 s6, s2, s6
	s_ashr_i32 s7, s6, 3
	s_and_b32 s6, s6, -8
	s_sub_i32 s6, s2, s6
	s_cmp_lt_i32 s6, 0
	s_movk_i32 s8, 0x161
	s_cselect_b32 s8, s8, 0x160
	s_mul_i32 s6, s6, s8
	s_add_i32 s6, s6, s7
	s_mul_hi_i32 s7, s6, 0x2e8ba2e9
	s_lshr_b32 s8, s7, 31
	s_ashr_i32 s7, s7, 5
	s_add_i32 s7, s7, s8
	s_lshl_b32 s8, s7, 3
	s_sub_i32 s9, 0x80, s8
	s_min_i32 s9, s9, 8
	s_abs_i32 s9, s9
	s_sub_i32 s10, 0, s9
	s_mulk_i32 s7, 0xb0
	s_sub_i32 s6, s6, s7
	s_ashr_i32 s7, s6, 31
	s_abs_i32 s6, s6
	s_mov_b32 s11, 0x1fffffc0
	s_mul_i32 s10, s10, s11
	s_mul_hi_u32 s10, s11, s10
	s_add_i32 s11, s11, s10
	s_mul_hi_u32 s10, s6, s11
	s_mul_i32 s10, s10, s9
	s_sub_i32 s6, s6, s10
	s_sub_i32 s10, s6, s9
	s_cmp_ge_u32 s6, s9
	s_cselect_b32 s6, s10, s6
	s_sub_i32 s10, s6, s9
	s_cmp_ge_u32 s6, s9
	s_cselect_b32 s6, s10, s6
	s_xor_b32 s6, s6, s7
	s_sub_i32 s6, s6, s7
	s_add_i32 s8, s8, s6
	v_lshl_add_u32 v4, s8, 8, v1
	v_readlane_b32 s6, v254, 63
	v_ashrrev_i32_e32 v5, 31, v4
	v_readlane_b32 s7, v255, 0
	v_mov_b32_e32 v2, s4
	s_add_u32 s2, s2, s88
	v_lshl_add_u64 v[4:5], v[4:5], 4, s[6:7]
	global_load_dwordx4 v[92:95], v[4:5], off
	s_addc_u32 s3, s3, s5
	v_mov_b64_e32 v[4:5], 0xaff
	v_cmp_gt_i64_e32 vcc, s[2:3], v[4:5]
	s_cbranch_vccnz .LBB0_718
;     __host__ __device__ bool next(int i, Unit& u) const {
;         const long L = (long)i * G + c; if (L >= nwg) return false;
;         int wgid = (int)L; { const int q = nwg / NXCD, r = nwg % NXCD, xcd = wgid % NXCD, off = wgid / NXCD; wgid = (xcd < r ? xcd * (q + 1) : r * (q + 1) + (xcd - r) * q) + off; }
;         const int nig = WGM * nN, gid = wgid / nig, fm = gid * WGM, gsz = (nM - fm) < WGM ? (nM - fm) : WGM;
;         u.pm = fm + ((wgid % nig) % gsz); u.pn = (wgid % nig) / gsz; u.idx = i; return true;
; template <class Sched> __device__ __forceinline__ void stage_scales(PG8_LAS unsigned char* lds, const Sched& S, const float* rs, bool cols, int ldil, int tid) {
;     ...
;     if (tid < 256) { const int lper = 8 - ldil, c = tid, tm = ((c & ((1 << lper) - 1)) << ldil) + (c >> lper);
;         float eps = 1e-6f; asm volatile("" : "+s"(eps));
;         for (int i = 0; i < 16 && S.next(i, u); ++i) { const f32x4 a = *(const f32x4*)(rs + 4 * (size_t)(cols ? u.pn * BM + tm : u.pm * BM + tid));
;             tab[i * 256 + tid] = __builtin_amdgcn_rsqf(((a[0] + a[1]) + (a[2] + a[3])) * (1.0f / 1024.0f) + eps); } }
	s_ashr_i32 s6, s2, 31
	s_lshr_b32 s6, s6, 29
	s_add_i32 s6, s2, s6
	s_ashr_i32 s7, s6, 3
	s_and_b32 s6, s6, -8
	s_sub_i32 s6, s2, s6
	s_cmp_lt_i32 s6, 0
	s_movk_i32 s8, 0x161
	s_cselect_b32 s8, s8, 0x160
	s_mul_i32 s6, s6, s8
	s_add_i32 s6, s6, s7
	s_mul_hi_i32 s7, s6, 0x2e8ba2e9
	s_lshr_b32 s8, s7, 31
	s_ashr_i32 s7, s7, 5
	s_add_i32 s7, s7, s8
	s_lshl_b32 s8, s7, 3
	s_sub_i32 s9, 0x80, s8
	s_min_i32 s9, s9, 8
	s_abs_i32 s9, s9
	s_sub_i32 s10, 0, s9
	s_mulk_i32 s7, 0xb0
	s_sub_i32 s6, s6, s7
	s_ashr_i32 s7, s6, 31
	s_abs_i32 s6, s6
	s_mov_b32 s11, 0x1fffffc0
	s_mul_i32 s10, s10, s11
	s_mul_hi_u32 s10, s11, s10
	s_add_i32 s11, s11, s10
	s_mul_hi_u32 s10, s6, s11
	s_mul_i32 s10, s10, s9
	s_sub_i32 s6, s6, s10
	s_sub_i32 s10, s6, s9
	s_cmp_ge_u32 s6, s9
	s_cselect_b32 s6, s10, s6
	s_sub_i32 s10, s6, s9
	s_cmp_ge_u32 s6, s9
	s_cselect_b32 s6, s10, s6
	s_xor_b32 s6, s6, s7
	s_sub_i32 s6, s6, s7
	s_add_i32 s8, s8, s6
	v_lshl_add_u32 v4, s8, 8, v1
	v_readlane_b32 s6, v254, 63
	v_ashrrev_i32_e32 v5, 31, v4
	v_readlane_b32 s7, v255, 0
	v_mov_b32_e32 v2, s4
	s_add_u32 s2, s2, s88
	v_lshl_add_u64 v[4:5], v[4:5], 4, s[6:7]
	global_load_dwordx4 v[96:99], v[4:5], off
	s_addc_u32 s3, s3, s5
	v_mov_b64_e32 v[4:5], 0xaff
	v_cmp_gt_i64_e32 vcc, s[2:3], v[4:5]
	s_cbranch_vccnz .LBB0_718
	s_ashr_i32 s6, s2, 31
	s_lshr_b32 s6, s6, 29
	s_add_i32 s6, s2, s6
	s_ashr_i32 s7, s6, 3
	s_and_b32 s6, s6, -8
	s_sub_i32 s6, s2, s6
	s_cmp_lt_i32 s6, 0
	s_movk_i32 s8, 0x161
	s_cselect_b32 s8, s8, 0x160
	s_mul_i32 s6, s6, s8
	s_add_i32 s6, s6, s7
	s_mul_hi_i32 s7, s6, 0x2e8ba2e9
	s_lshr_b32 s8, s7, 31
	s_ashr_i32 s7, s7, 5
	s_add_i32 s7, s7, s8
	s_lshl_b32 s8, s7, 3
	s_sub_i32 s9, 0x80, s8
	s_min_i32 s9, s9, 8
	s_abs_i32 s9, s9
	s_sub_i32 s10, 0, s9
	s_mulk_i32 s7, 0xb0
	s_sub_i32 s6, s6, s7
	s_ashr_i32 s7, s6, 31
	s_abs_i32 s6, s6
	s_mov_b32 s11, 0x1fffffc0
	s_mul_i32 s10, s10, s11
	s_mul_hi_u32 s10, s11, s10
	s_add_i32 s11, s11, s10
	s_mul_hi_u32 s10, s6, s11
	s_mul_i32 s10, s10, s9
	s_sub_i32 s6, s6, s10
	s_sub_i32 s10, s6, s9
	s_cmp_ge_u32 s6, s9
	s_cselect_b32 s6, s10, s6
	s_sub_i32 s10, s6, s9
	s_cmp_ge_u32 s6, s9
	s_cselect_b32 s6, s10, s6
	s_xor_b32 s6, s6, s7
	s_sub_i32 s6, s6, s7
	s_add_i32 s8, s8, s6
	v_lshl_add_u32 v4, s8, 8, v1
	v_readlane_b32 s6, v254, 63
	v_ashrrev_i32_e32 v5, 31, v4
	v_readlane_b32 s7, v255, 0
	v_mov_b32_e32 v2, s4
	s_add_u32 s2, s2, s88
	v_lshl_add_u64 v[4:5], v[4:5], 4, s[6:7]
	global_load_dwordx4 v[100:103], v[4:5], off
	s_addc_u32 s3, s3, s5
	v_mov_b64_e32 v[4:5], 0xaff
	v_cmp_gt_i64_e32 vcc, s[2:3], v[4:5]
	s_cbranch_vccnz .LBB0_718
	s_ashr_i32 s6, s2, 31
	s_lshr_b32 s6, s6, 29
	s_add_i32 s6, s2, s6
	s_ashr_i32 s7, s6, 3
	s_and_b32 s6, s6, -8
	s_sub_i32 s6, s2, s6
	s_cmp_lt_i32 s6, 0
	s_movk_i32 s8, 0x161
	s_cselect_b32 s8, s8, 0x160
	s_mul_i32 s6, s6, s8
	s_add_i32 s6, s6, s7
	s_mul_hi_i32 s7, s6, 0x2e8ba2e9
	s_lshr_b32 s8, s7, 31
	s_ashr_i32 s7, s7, 5
	s_add_i32 s7, s7, s8
	s_lshl_b32 s8, s7, 3
	s_sub_i32 s9, 0x80, s8
	s_min_i32 s9, s9, 8
	s_abs_i32 s9, s9
	s_sub_i32 s10, 0, s9
	s_mulk_i32 s7, 0xb0
	s_sub_i32 s6, s6, s7
	s_ashr_i32 s7, s6, 31
	s_abs_i32 s6, s6
	s_mov_b32 s11, 0x1fffffc0
	s_mul_i32 s10, s10, s11
	s_mul_hi_u32 s10, s11, s10
	s_add_i32 s11, s11, s10
	s_mul_hi_u32 s10, s6, s11
	s_mul_i32 s10, s10, s9
	s_sub_i32 s6, s6, s10
	s_sub_i32 s10, s6, s9
	s_cmp_ge_u32 s6, s9
	s_cselect_b32 s6, s10, s6
	s_sub_i32 s10, s6, s9
	s_cmp_ge_u32 s6, s9
	s_cselect_b32 s6, s10, s6
	s_xor_b32 s6, s6, s7
	s_sub_i32 s6, s6, s7
	s_add_i32 s8, s8, s6
	v_lshl_add_u32 v4, s8, 8, v1
	v_readlane_b32 s6, v254, 63
	v_ashrrev_i32_e32 v5, 31, v4
	v_readlane_b32 s7, v255, 0
	v_mov_b32_e32 v2, s4
	s_add_u32 s2, s2, s88
	v_lshl_add_u64 v[4:5], v[4:5], 4, s[6:7]
	global_load_dwordx4 v[104:107], v[4:5], off
	s_addc_u32 s3, s3, s5
	v_mov_b64_e32 v[4:5], 0xaff
	v_cmp_gt_i64_e32 vcc, s[2:3], v[4:5]
	s_cbranch_vccnz .LBB0_718
	s_ashr_i32 s6, s2, 31
	s_lshr_b32 s6, s6, 29
	s_add_i32 s6, s2, s6
	s_ashr_i32 s7, s6, 3
	s_and_b32 s6, s6, -8
	s_sub_i32 s6, s2, s6
	s_cmp_lt_i32 s6, 0
	s_movk_i32 s8, 0x161
	s_cselect_b32 s8, s8, 0x160
	s_mul_i32 s6, s6, s8
	s_add_i32 s6, s6, s7
	s_mul_hi_i32 s7, s6, 0x2e8ba2e9
	s_lshr_b32 s8, s7, 31
	s_ashr_i32 s7, s7, 5
	s_add_i32 s7, s7, s8
	s_lshl_b32 s8, s7, 3
	s_sub_i32 s9, 0x80, s8
	s_min_i32 s9, s9, 8
	s_abs_i32 s9, s9
	s_sub_i32 s10, 0, s9
	s_mulk_i32 s7, 0xb0
	s_sub_i32 s6, s6, s7
	s_ashr_i32 s7, s6, 31
	s_abs_i32 s6, s6
	s_mov_b32 s11, 0x1fffffc0
	s_mul_i32 s10, s10, s11
	s_mul_hi_u32 s10, s11, s10
	s_add_i32 s11, s11, s10
	s_mul_hi_u32 s10, s6, s11
	s_mul_i32 s10, s10, s9
	s_sub_i32 s6, s6, s10
	s_sub_i32 s10, s6, s9
	s_cmp_ge_u32 s6, s9
	s_cselect_b32 s6, s10, s6
	s_sub_i32 s10, s6, s9
	s_cmp_ge_u32 s6, s9
	s_cselect_b32 s6, s10, s6
	s_xor_b32 s6, s6, s7
	s_sub_i32 s6, s6, s7
	s_add_i32 s8, s8, s6
	v_lshl_add_u32 v4, s8, 8, v1
	v_readlane_b32 s6, v254, 63
	v_ashrrev_i32_e32 v5, 31, v4
	v_readlane_b32 s7, v255, 0
	v_mov_b32_e32 v2, s4
	s_add_u32 s2, s2, s88
	v_lshl_add_u64 v[4:5], v[4:5], 4, s[6:7]
	global_load_dwordx4 v[108:111], v[4:5], off
	s_addc_u32 s3, s3, s5
	v_mov_b64_e32 v[4:5], 0xaff
	v_cmp_gt_i64_e32 vcc, s[2:3], v[4:5]
	s_cbranch_vccnz .LBB0_718
;     __host__ __device__ bool next(int i, Unit& u) const {
;         const long L = (long)i * G + c; if (L >= nwg) return false;
;         int wgid = (int)L; { const int q = nwg / NXCD, r = nwg % NXCD, xcd = wgid % NXCD, off = wgid / NXCD; wgid = (xcd < r ? xcd * (q + 1) : r * (q + 1) + (xcd - r) * q) + off; }
;         const int nig = WGM * nN, gid = wgid / nig, fm = gid * WGM, gsz = (nM - fm) < WGM ? (nM - fm) : WGM;
;         u.pm = fm + ((wgid % nig) % gsz); u.pn = (wgid % nig) / gsz; u.idx = i; return true;
; template <class Sched> __device__ __forceinline__ void stage_scales(PG8_LAS unsigned char* lds, const Sched& S, const float* rs, bool cols, int ldil, int tid) {
;     ...
;     if (tid < 256) { const int lper = 8 - ldil, c = tid, tm = ((c & ((1 << lper) - 1)) << ldil) + (c >> lper);
;         float eps = 1e-6f; asm volatile("" : "+s"(eps));
;         for (int i = 0; i < 16 && S.next(i, u); ++i) { const f32x4 a = *(const f32x4*)(rs + 4 * (size_t)(cols ? u.pn * BM + tm : u.pm * BM + tid));
;             tab[i * 256 + tid] = __builtin_amdgcn_rsqf(((a[0] + a[1]) + (a[2] + a[3])) * (1.0f / 1024.0f) + eps); } }
	s_ashr_i32 s6, s2, 31
	s_lshr_b32 s6, s6, 29
	s_add_i32 s6, s2, s6
	s_ashr_i32 s7, s6, 3
	s_and_b32 s6, s6, -8
	s_sub_i32 s6, s2, s6
	s_cmp_lt_i32 s6, 0
	s_movk_i32 s8, 0x161
	s_cselect_b32 s8, s8, 0x160
	s_mul_i32 s6, s6, s8
	s_add_i32 s6, s6, s7
	s_mul_hi_i32 s7, s6, 0x2e8ba2e9
	s_lshr_b32 s8, s7, 31
	s_ashr_i32 s7, s7, 5
	s_add_i32 s7, s7, s8
	s_lshl_b32 s8, s7, 3
	s_sub_i32 s9, 0x80, s8
	s_min_i32 s9, s9, 8
	s_abs_i32 s9, s9
	s_sub_i32 s10, 0, s9
	s_mulk_i32 s7, 0xb0
	s_sub_i32 s6, s6, s7
	s_ashr_i32 s7, s6, 31
	s_abs_i32 s6, s6
	s_mov_b32 s11, 0x1fffffc0
	s_mul_i32 s10, s10, s11
	s_mul_hi_u32 s10, s11, s10
	s_add_i32 s11, s11, s10
	s_mul_hi_u32 s10, s6, s11
	s_mul_i32 s10, s10, s9
	s_sub_i32 s6, s6, s10
	s_sub_i32 s10, s6, s9
	s_cmp_ge_u32 s6, s9
	s_cselect_b32 s6, s10, s6
	s_sub_i32 s10, s6, s9
	s_cmp_ge_u32 s6, s9
	s_cselect_b32 s6, s10, s6
	s_xor_b32 s6, s6, s7
	s_sub_i32 s6, s6, s7
	s_add_i32 s8, s8, s6
	v_lshl_add_u32 v4, s8, 8, v1
	v_readlane_b32 s6, v254, 63
	v_ashrrev_i32_e32 v5, 31, v4
	v_readlane_b32 s7, v255, 0
	v_mov_b32_e32 v2, s4
	s_add_u32 s2, s2, s88
	v_lshl_add_u64 v[4:5], v[4:5], 4, s[6:7]
	global_load_dwordx4 v[112:115], v[4:5], off
	s_addc_u32 s3, s3, s5
	v_mov_b64_e32 v[4:5], 0xaff
	v_cmp_gt_i64_e32 vcc, s[2:3], v[4:5]
	s_cbranch_vccnz .LBB0_718
	s_ashr_i32 s6, s2, 31
	s_lshr_b32 s6, s6, 29
	s_add_i32 s6, s2, s6
	s_ashr_i32 s7, s6, 3
	s_and_b32 s6, s6, -8
	s_sub_i32 s6, s2, s6
	s_cmp_lt_i32 s6, 0
	s_movk_i32 s8, 0x161
	s_cselect_b32 s8, s8, 0x160
	s_mul_i32 s6, s6, s8
	s_add_i32 s6, s6, s7
	s_mul_hi_i32 s7, s6, 0x2e8ba2e9
	s_lshr_b32 s8, s7, 31
	s_ashr_i32 s7, s7, 5
	s_add_i32 s7, s7, s8
	s_lshl_b32 s8, s7, 3
	s_sub_i32 s9, 0x80, s8
	s_min_i32 s9, s9, 8
	s_abs_i32 s9, s9
	s_sub_i32 s10, 0, s9
	s_mulk_i32 s7, 0xb0
	s_sub_i32 s6, s6, s7
	s_ashr_i32 s7, s6, 31
	s_abs_i32 s6, s6
	s_mov_b32 s11, 0x1fffffc0
	s_mul_i32 s10, s10, s11
	s_mul_hi_u32 s10, s11, s10
	s_add_i32 s11, s11, s10
	s_mul_hi_u32 s10, s6, s11
	s_mul_i32 s10, s10, s9
	s_sub_i32 s6, s6, s10
	s_sub_i32 s10, s6, s9
	s_cmp_ge_u32 s6, s9
	s_cselect_b32 s6, s10, s6
	s_sub_i32 s10, s6, s9
	s_cmp_ge_u32 s6, s9
	s_cselect_b32 s6, s10, s6
	s_xor_b32 s6, s6, s7
	s_sub_i32 s6, s6, s7
	s_add_i32 s8, s8, s6
	v_lshl_add_u32 v4, s8, 8, v1
	v_readlane_b32 s6, v254, 63
	v_ashrrev_i32_e32 v5, 31, v4
	v_readlane_b32 s7, v255, 0
	v_mov_b32_e32 v2, s4
	s_add_u32 s2, s2, s88
	v_lshl_add_u64 v[4:5], v[4:5], 4, s[6:7]
	global_load_dwordx4 v[116:119], v[4:5], off
	s_addc_u32 s3, s3, s5
	v_mov_b64_e32 v[4:5], 0xaff
	v_cmp_gt_i64_e32 vcc, s[2:3], v[4:5]
	s_cbranch_vccnz .LBB0_718
	s_ashr_i32 s6, s2, 31
	s_lshr_b32 s6, s6, 29
	s_add_i32 s6, s2, s6
	s_ashr_i32 s7, s6, 3
	s_and_b32 s6, s6, -8
	s_sub_i32 s6, s2, s6
	s_cmp_lt_i32 s6, 0
	s_movk_i32 s8, 0x161
	s_cselect_b32 s8, s8, 0x160
	s_mul_i32 s6, s6, s8
	s_add_i32 s6, s6, s7
	s_mul_hi_i32 s7, s6, 0x2e8ba2e9
	s_lshr_b32 s8, s7, 31
	s_ashr_i32 s7, s7, 5
	s_add_i32 s7, s7, s8
	s_lshl_b32 s8, s7, 3
	s_sub_i32 s9, 0x80, s8
	s_min_i32 s9, s9, 8
	s_abs_i32 s9, s9
	s_sub_i32 s10, 0, s9
	s_mulk_i32 s7, 0xb0
	s_sub_i32 s6, s6, s7
	s_ashr_i32 s7, s6, 31
	s_abs_i32 s6, s6
	s_mov_b32 s11, 0x1fffffc0
	s_mul_i32 s10, s10, s11
	s_mul_hi_u32 s10, s11, s10
	s_add_i32 s11, s11, s10
	s_mul_hi_u32 s10, s6, s11
	s_mul_i32 s10, s10, s9
	s_sub_i32 s6, s6, s10
	s_sub_i32 s10, s6, s9
	s_cmp_ge_u32 s6, s9
	s_cselect_b32 s6, s10, s6
	s_sub_i32 s10, s6, s9
	s_cmp_ge_u32 s6, s9
	s_cselect_b32 s6, s10, s6
	s_xor_b32 s6, s6, s7
	s_sub_i32 s6, s6, s7
	s_add_i32 s8, s8, s6
	v_lshl_add_u32 v4, s8, 8, v1
	v_readlane_b32 s6, v254, 63
	v_ashrrev_i32_e32 v5, 31, v4
	v_readlane_b32 s7, v255, 0
	v_mov_b32_e32 v2, s4
	s_add_u32 s2, s2, s88
	v_lshl_add_u64 v[4:5], v[4:5], 4, s[6:7]
	global_load_dwordx4 v[120:123], v[4:5], off
	s_addc_u32 s3, s3, s5
	v_mov_b64_e32 v[4:5], 0xaff
	v_cmp_gt_i64_e32 vcc, s[2:3], v[4:5]
	s_cbranch_vccnz .LBB0_718
	s_ashr_i32 s3, s2, 31
	s_lshr_b32 s3, s3, 29
	s_add_i32 s3, s2, s3
	s_ashr_i32 s5, s3, 3
	s_and_b32 s3, s3, -8
	s_sub_i32 s2, s2, s3
	s_cmp_lt_i32 s2, 0
	s_movk_i32 s3, 0x161
	s_cselect_b32 s3, s3, 0x160
	s_mul_i32 s2, s2, s3
	s_add_i32 s2, s2, s5
	s_mul_hi_i32 s3, s2, 0x2e8ba2e9
	s_lshr_b32 s5, s3, 31
	s_ashr_i32 s3, s3, 5
	s_add_i32 s3, s3, s5
	s_lshl_b32 s5, s3, 3
	s_sub_i32 s6, 0x80, s5
	s_min_i32 s6, s6, 8
	s_abs_i32 s6, s6
	s_sub_i32 s7, 0, s6
	s_mulk_i32 s3, 0xb0
	s_sub_i32 s2, s2, s3
	s_ashr_i32 s3, s2, 31
	s_abs_i32 s2, s2
	s_mov_b32 s8, 0x1fffffc0
	s_mul_i32 s7, s7, s8
	s_mul_hi_u32 s7, s8, s7
	s_add_i32 s8, s8, s7
	s_mul_hi_u32 s7, s2, s8
	s_mul_i32 s7, s7, s6
	s_sub_i32 s2, s2, s7
	s_sub_i32 s7, s2, s6
	s_cmp_ge_u32 s2, s6
	s_cselect_b32 s2, s7, s2
	s_sub_i32 s7, s2, s6
	s_cmp_ge_u32 s2, s6
	s_cselect_b32 s2, s7, s2
	s_xor_b32 s2, s2, s3
	s_sub_i32 s2, s2, s3
	s_add_i32 s5, s5, s2
	v_lshl_add_u32 v4, s5, 8, v1
	v_readlane_b32 s2, v254, 63
	v_ashrrev_i32_e32 v5, 31, v4
	v_readlane_b32 s3, v255, 0
	s_nop 1
	v_lshl_add_u64 v[4:5], v[4:5], 4, s[2:3]
	global_load_dwordx4 v[124:127], v[4:5], off

; #define PG8_STAGE(bufoff, gbase, voff) do { _Pragma("unroll") for (int _i = 0; _i < 2; ++_i) \
;         __builtin_amdgcn_global_load_lds((const unsigned*)((const char*)(gbase) + (voff)[_i]), (PG8_LAS unsigned*)(lds + (bufoff) + ldsw + _i * 8192), 16, 0, 0); } while (0)
; #define PG8_LDA(dst, b, h) do { _Pragma("unroll") for (int m = 0; m < 4; ++m) _Pragma("unroll") for (int k = 0; k < 2; ++k) dst[m][k] = *(const PG8_LAS bf16x8*)(lds + PG8_SA(b, h) + aoff + m * 2048 + k * 1024); } while (0)
; #define PG8_LDB(dst, b, h) do { _Pragma("unroll") for (int n = 0; n < 2; ++n) _Pragma("unroll") for (int k = 0; k < 2; ++k) dst[n][k] = *(const PG8_LAS bf16x8*)(lds + PG8_SB(b, h) + boff + n * 2048 + k * 1024); } while (0)
; #define PG8_MMA(ai, bj, At, Bt) do { __builtin_amdgcn_s_setprio(1); _Pragma("unroll") for (int m = 0; m < 4; ++m) _Pragma("unroll") for (int n = 0; n < 2; ++n) _Pragma("unroll") for (int k = 0; k < 2; ++k) \
;         acc[ai][bj][m][n] = __builtin_amdgcn_mfma_f32_16x16x32_bf16(Bt[n][k], At[m][k], acc[ai][bj][m][n], 0, 0, 0); __builtin_amdgcn_s_setprio(0); } while (0)
; #define PG8_WAIT_V(n) asm volatile("s_waitcnt vmcnt(" #n ")" ::: "memory")
; #define PG8_WAIT_L(n) asm volatile("s_waitcnt lgkmcnt(" #n ")" ::: "memory")
; #define PG8_BAR __builtin_amdgcn_s_barrier()
; #define PG8_SCHED __builtin_amdgcn_sched_barrier(0)
; template <class Epi, class Sched, bool ALIGN_EPI = false, bool SP2 = false>
; __device__ __forceinline__ void gemm_phase(PG8_LAS unsigned char* lds, const Gemm g, const Sched& S, const Epi& E, const int tid) {
;     ...
;             PG8_LDB(B0, 0, 0); PG8_LDB(B1, 0, 1); PG8_SCHED; PG8_LDA(At, 0, 0); PG8_STAGE(PG8_SA(1, 1), a1 + hstep, voffA);
;             PG8_WAIT_V(8); PG8_WAIT_L(0); PG8_BAR; PG8_MMA(0, 0, At, B0); PG8_MMA(0, 1, At, B1); PG8_BAR; PG8_SCHED;
;             PG8_LDA(At, 0, 1); PG8_STAGE(PG8_SB(0, 0), b2, voffB); PG8_STAGE(PG8_SB(0, 1), b2, voffB1); PG8_STAGE(PG8_SA(0, 0), a2, voffA);
;             PG8_WAIT_V(8); PG8_WAIT_L(0); PG8_BAR; PG8_MMA(1, 0, At, B0); PG8_MMA(1, 1, At, B1); PG8_BAR; PG8_SCHED;
.LBB0_724:
.LBB0_726:
	s_add_u32 s46, s46, 0x40080
	s_addc_u32 s47, s47, 0
	s_add_u32 s52, s52, 0x100
	s_addc_u32 s53, s53, 0
	s_mov_b32 s62, -2
	s_add_u32 s36, s46, 0xfffc0080
	s_addc_u32 s37, s47, -1
	s_add_i32 s63, 0, 0x10000
	s_cmp_eq_u32 s62, 12
	s_cselect_b32 s37, s11, s37
	s_cselect_b32 s36, s59, s36
	v_add_u32_e32 v148, s63, v151
	s_cselect_b32 s73, s9, s53
	s_cselect_b32 s72, s60, s52
	s_add_i32 s68, 0, 0x14000
	ds_read_b128 v[144:147], v148
	ds_read_b128 v[156:159], v148 offset:1024
	ds_read_b128 v[160:163], v148 offset:2048
	ds_read_b128 v[164:167], v148 offset:3072
	v_add_u32_e32 v148, s68, v151
	ds_read_b128 v[168:171], v148
	ds_read_b128 v[172:175], v148 offset:1024
	ds_read_b128 v[176:179], v148 offset:2048
	ds_read_b128 v[180:183], v148 offset:3072
	v_lshl_add_u64 v[148:149], s[46:47], 0, v[140:141]
	s_add_i32 m0, s43, 0xc000
	ds_read_b128 v[184:187], v154
	ds_read_b128 v[188:191], v154 offset:1024
	ds_read_b128 v[192:195], v154 offset:2048
	ds_read_b128 v[196:199], v154 offset:3072
	ds_read_b128 v[212:215], v154 offset:4096
	ds_read_b128 v[216:219], v154 offset:5120
	ds_read_b128 v[220:223], v154 offset:6144
	ds_read_b128 v[224:227], v154 offset:7168
	global_load_lds_dwordx4 v[148:149], off
	v_lshl_add_u64 v[148:149], s[46:47], 0, v[142:143]
	s_add_i32 m0, s43, 0xe000
	s_nop 0
	global_load_lds_dwordx4 v[148:149], off
	s_waitcnt vmcnt(8)
	s_waitcnt lgkmcnt(0)
	s_barrier
	s_setprio 1
	s_waitcnt lgkmcnt(0)
	v_mfma_f32_16x16x32_bf16 v[128:131], v[144:147], v[184:187], 0
	v_mfma_f32_16x16x32_bf16 v[120:123], v[160:163], v[184:187], 0
	v_mfma_f32_16x16x32_bf16 v[112:115], v[144:147], v[192:195], 0
	v_mfma_f32_16x16x32_bf16 v[104:107], v[160:163], v[192:195], 0
	v_mfma_f32_16x16x32_bf16 v[96:99], v[144:147], v[212:215], 0
	v_mfma_f32_16x16x32_bf16 v[88:91], v[160:163], v[212:215], 0
	v_mfma_f32_16x16x32_bf16 v[80:83], v[144:147], v[220:223], 0
	v_mfma_f32_16x16x32_bf16 v[72:75], v[160:163], v[220:223], 0
	v_mfma_f32_16x16x32_bf16 v[128:131], v[156:159], v[188:191], v[128:131]
	v_mfma_f32_16x16x32_bf16 v[120:123], v[164:167], v[188:191], v[120:123]
	v_mfma_f32_16x16x32_bf16 v[112:115], v[156:159], v[196:199], v[112:115]
	v_mfma_f32_16x16x32_bf16 v[104:107], v[164:167], v[196:199], v[104:107]
	v_mfma_f32_16x16x32_bf16 v[96:99], v[156:159], v[216:219], v[96:99]
	v_mfma_f32_16x16x32_bf16 v[88:91], v[164:167], v[216:219], v[88:91]
	v_mfma_f32_16x16x32_bf16 v[80:83], v[156:159], v[224:227], v[80:83]
	v_mfma_f32_16x16x32_bf16 v[72:75], v[164:167], v[224:227], v[72:75]
	s_setprio 0
	s_setprio 1
	v_mfma_f32_16x16x32_bf16 v[124:127], v[168:171], v[184:187], 0
	v_mfma_f32_16x16x32_bf16 v[116:119], v[176:179], v[184:187], 0
	v_mfma_f32_16x16x32_bf16 v[108:111], v[168:171], v[192:195], 0
	v_mfma_f32_16x16x32_bf16 v[100:103], v[176:179], v[192:195], 0
	v_mfma_f32_16x16x32_bf16 v[92:95], v[168:171], v[212:215], 0
	v_mfma_f32_16x16x32_bf16 v[84:87], v[176:179], v[212:215], 0
	v_mfma_f32_16x16x32_bf16 v[76:79], v[168:171], v[220:223], 0
	v_mfma_f32_16x16x32_bf16 v[68:71], v[176:179], v[220:223], 0
	v_mfma_f32_16x16x32_bf16 v[124:127], v[172:175], v[188:191], v[124:127]
	v_mfma_f32_16x16x32_bf16 v[116:119], v[180:183], v[188:191], v[116:119]
	v_mfma_f32_16x16x32_bf16 v[108:111], v[172:175], v[196:199], v[108:111]
	v_mfma_f32_16x16x32_bf16 v[100:103], v[180:183], v[196:199], v[100:103]
	v_mfma_f32_16x16x32_bf16 v[92:95], v[172:175], v[216:219], v[92:95]
	v_mfma_f32_16x16x32_bf16 v[84:87], v[180:183], v[216:219], v[84:87]
	v_mfma_f32_16x16x32_bf16 v[76:79], v[172:175], v[224:227], v[76:79]
	v_mfma_f32_16x16x32_bf16 v[68:71], v[180:183], v[224:227], v[68:71]
	s_setprio 0
	s_barrier
	s_add_i32 s63, s63, s33
	v_lshl_add_u64 v[148:149], s[72:73], 0, v[2:3]
	s_mov_b32 m0, s63
	ds_read_b128 v[184:187], v154 offset:16384
	ds_read_b128 v[188:191], v154 offset:17408
	ds_read_b128 v[192:195], v154 offset:18432
	ds_read_b128 v[196:199], v154 offset:19456
	ds_read_b128 v[212:215], v154 offset:20480
	ds_read_b128 v[216:219], v154 offset:21504
	ds_read_b128 v[220:223], v154 offset:22528
	ds_read_b128 v[224:227], v154 offset:23552
	global_load_lds_dwordx4 v[148:149], off
	v_lshl_add_u64 v[200:201], s[72:73], 0, v[132:133]
	s_add_i32 m0, s63, 0x2000
	s_add_i32 s63, s68, s33
	global_load_lds_dwordx4 v[200:201], off
	v_lshl_add_u64 v[202:203], s[72:73], 0, v[136:137]
	s_mov_b32 m0, s63
	v_lshl_add_u64 v[204:205], s[72:73], 0, v[0:1]
	global_load_lds_dwordx4 v[202:203], off
	s_add_i32 m0, s63, 0x2000
	v_lshl_add_u64 v[208:209], s[36:37], 0, v[138:139]
	global_load_lds_dwordx4 v[204:205], off
	s_mov_b32 m0, s43
	v_lshl_add_u64 v[210:211], s[36:37], 0, v[134:135]
	global_load_lds_dwordx4 v[208:209], off
	s_mov_b32 m0, s45
	s_nop 0
	global_load_lds_dwordx4 v[210:211], off
	s_waitcnt vmcnt(8)
	s_waitcnt lgkmcnt(0)
	s_barrier
; #define PG8_STAGE(bufoff, gbase, voff) do { _Pragma("unroll") for (int _i = 0; _i < 2; ++_i) \
;         __builtin_amdgcn_global_load_lds((const unsigned*)((const char*)(gbase) + (voff)[_i]), (PG8_LAS unsigned*)(lds + (bufoff) + ldsw + _i * 8192), 16, 0, 0); } while (0)
; #define PG8_LDA(dst, b, h) do { _Pragma("unroll") for (int m = 0; m < 4; ++m) _Pragma("unroll") for (int k = 0; k < 2; ++k) dst[m][k] = *(const PG8_LAS bf16x8*)(lds + PG8_SA(b, h) + aoff + m * 2048 + k * 1024); } while (0)
; #define PG8_LDB(dst, b, h) do { _Pragma("unroll") for (int n = 0; n < 2; ++n) _Pragma("unroll") for (int k = 0; k < 2; ++k) dst[n][k] = *(const PG8_LAS bf16x8*)(lds + PG8_SB(b, h) + boff + n * 2048 + k * 1024); } while (0)
; #define PG8_MMA(ai, bj, At, Bt) do { __builtin_amdgcn_s_setprio(1); _Pragma("unroll") for (int m = 0; m < 4; ++m) _Pragma("unroll") for (int n = 0; n < 2; ++n) _Pragma("unroll") for (int k = 0; k < 2; ++k) \
;         acc[ai][bj][m][n] = __builtin_amdgcn_mfma_f32_16x16x32_bf16(Bt[n][k], At[m][k], acc[ai][bj][m][n], 0, 0, 0); __builtin_amdgcn_s_setprio(0); } while (0)
; #define PG8_WAIT_V(n) asm volatile("s_waitcnt vmcnt(" #n ")" ::: "memory")
; #define PG8_WAIT_L(n) asm volatile("s_waitcnt lgkmcnt(" #n ")" ::: "memory")
; #define PG8_BAR __builtin_amdgcn_s_barrier()
; #define PG8_SCHED __builtin_amdgcn_sched_barrier(0)
; template <class Epi, class Sched, bool ALIGN_EPI = false, bool SP2 = false>
; __device__ __forceinline__ void gemm_phase(PG8_LAS unsigned char* lds, const Gemm g, const Sched& S, const Epi& E, const int tid) {
;     ...
;             PG8_WAIT_V(8); PG8_WAIT_L(0); PG8_BAR; PG8_MMA(1, 0, At, B0); PG8_MMA(1, 1, At, B1); PG8_BAR; PG8_SCHED;
;             PG8_LDB(B0, 1, 0); PG8_LDB(B1, 1, 1); PG8_SCHED; PG8_LDA(At, 1, 0); PG8_STAGE(PG8_SA(0, 1), a2 + hstep, voffA);
;             PG8_WAIT_V(8); PG8_WAIT_L(0); PG8_BAR; PG8_MMA(0, 0, At, B0); PG8_MMA(0, 1, At, B1); PG8_BAR; PG8_SCHED;
	s_setprio 1
	s_waitcnt lgkmcnt(0)
	v_mfma_f32_16x16x32_bf16 v[64:67], v[144:147], v[184:187], 0
	v_mfma_f32_16x16x32_bf16 v[56:59], v[160:163], v[184:187], 0
	v_mfma_f32_16x16x32_bf16 v[48:51], v[144:147], v[192:195], 0
	v_mfma_f32_16x16x32_bf16 v[40:43], v[160:163], v[192:195], 0
	v_mfma_f32_16x16x32_bf16 v[32:35], v[144:147], v[212:215], 0
	v_mfma_f32_16x16x32_bf16 v[24:27], v[160:163], v[212:215], 0
	v_mfma_f32_16x16x32_bf16 v[16:19], v[144:147], v[220:223], 0
	v_mfma_f32_16x16x32_bf16 v[8:11], v[160:163], v[220:223], 0
	v_mfma_f32_16x16x32_bf16 v[64:67], v[156:159], v[188:191], v[64:67]
	v_mfma_f32_16x16x32_bf16 v[56:59], v[164:167], v[188:191], v[56:59]
	v_mfma_f32_16x16x32_bf16 v[48:51], v[156:159], v[196:199], v[48:51]
	v_mfma_f32_16x16x32_bf16 v[40:43], v[164:167], v[196:199], v[40:43]
	v_mfma_f32_16x16x32_bf16 v[32:35], v[156:159], v[216:219], v[32:35]
	v_mfma_f32_16x16x32_bf16 v[24:27], v[164:167], v[216:219], v[24:27]
	v_mfma_f32_16x16x32_bf16 v[16:19], v[156:159], v[224:227], v[16:19]
	v_mfma_f32_16x16x32_bf16 v[8:11], v[164:167], v[224:227], v[8:11]
	s_setprio 0
	s_setprio 1
	v_mfma_f32_16x16x32_bf16 v[60:63], v[168:171], v[184:187], 0
	v_mfma_f32_16x16x32_bf16 v[52:55], v[176:179], v[184:187], 0
	v_mfma_f32_16x16x32_bf16 v[44:47], v[168:171], v[192:195], 0
	v_mfma_f32_16x16x32_bf16 v[36:39], v[176:179], v[192:195], 0
	v_mfma_f32_16x16x32_bf16 v[28:31], v[168:171], v[212:215], 0
	v_mfma_f32_16x16x32_bf16 v[20:23], v[176:179], v[212:215], 0
	v_mfma_f32_16x16x32_bf16 v[12:15], v[168:171], v[220:223], 0
	v_mfma_f32_16x16x32_bf16 v[4:7], v[176:179], v[220:223], 0
	v_mfma_f32_16x16x32_bf16 v[60:63], v[172:175], v[188:191], v[60:63]
	v_mfma_f32_16x16x32_bf16 v[52:55], v[180:183], v[188:191], v[52:55]
	v_mfma_f32_16x16x32_bf16 v[44:47], v[172:175], v[196:199], v[44:47]
	v_mfma_f32_16x16x32_bf16 v[36:39], v[180:183], v[196:199], v[36:39]
	v_mfma_f32_16x16x32_bf16 v[28:31], v[172:175], v[216:219], v[28:31]
	v_mfma_f32_16x16x32_bf16 v[20:23], v[180:183], v[216:219], v[20:23]
	v_mfma_f32_16x16x32_bf16 v[12:15], v[172:175], v[224:227], v[12:15]
	v_mfma_f32_16x16x32_bf16 v[4:7], v[180:183], v[224:227], v[4:7]
	s_setprio 0
	s_barrier
	s_add_i32 s63, 0, 0x18000
	v_add_u32_e32 v155, s63, v151
	s_add_i32 s68, 0, 0x1c000
	ds_read_b128 v[144:147], v155
	ds_read_b128 v[156:159], v155 offset:1024
	ds_read_b128 v[160:163], v155 offset:2048
	ds_read_b128 v[164:167], v155 offset:3072
	v_add_u32_e32 v155, s68, v151
	ds_read_b128 v[168:171], v155
	ds_read_b128 v[172:175], v155 offset:1024
	ds_read_b128 v[176:179], v155 offset:2048
	ds_read_b128 v[180:183], v155 offset:3072
	s_add_u32 s36, s36, 0x40000
	s_addc_u32 s37, s37, 0
	s_mov_b32 m0, s48
	v_lshl_add_u64 v[228:229], s[36:37], 0, v[138:139]
	ds_read_b128 v[184:187], v154 offset:32768
	ds_read_b128 v[188:191], v154 offset:33792
	ds_read_b128 v[192:195], v154 offset:34816
	ds_read_b128 v[196:199], v154 offset:35840
	ds_read_b128 v[212:215], v154 offset:36864
	ds_read_b128 v[216:219], v154 offset:37888
	ds_read_b128 v[220:223], v154 offset:38912
	ds_read_b128 v[224:227], v154 offset:39936
	global_load_lds_dwordx4 v[228:229], off
	v_lshl_add_u64 v[228:229], s[36:37], 0, v[134:135]
	s_mov_b32 m0, s49
	s_nop 0
	global_load_lds_dwordx4 v[228:229], off
	s_waitcnt vmcnt(8)
	s_waitcnt lgkmcnt(0)
	s_barrier
	s_setprio 1
	s_waitcnt lgkmcnt(0)
	v_mfma_f32_16x16x32_bf16 v[128:131], v[144:147], v[184:187], v[128:131]
	v_mfma_f32_16x16x32_bf16 v[120:123], v[160:163], v[184:187], v[120:123]
	v_mfma_f32_16x16x32_bf16 v[112:115], v[144:147], v[192:195], v[112:115]
	v_mfma_f32_16x16x32_bf16 v[104:107], v[160:163], v[192:195], v[104:107]
	v_mfma_f32_16x16x32_bf16 v[96:99], v[144:147], v[212:215], v[96:99]
	v_mfma_f32_16x16x32_bf16 v[88:91], v[160:163], v[212:215], v[88:91]
	v_mfma_f32_16x16x32_bf16 v[80:83], v[144:147], v[220:223], v[80:83]
	v_mfma_f32_16x16x32_bf16 v[72:75], v[160:163], v[220:223], v[72:75]
	v_mfma_f32_16x16x32_bf16 v[128:131], v[156:159], v[188:191], v[128:131]
	v_mfma_f32_16x16x32_bf16 v[120:123], v[164:167], v[188:191], v[120:123]
	v_mfma_f32_16x16x32_bf16 v[112:115], v[156:159], v[196:199], v[112:115]
	v_mfma_f32_16x16x32_bf16 v[104:107], v[164:167], v[196:199], v[104:107]
	v_mfma_f32_16x16x32_bf16 v[96:99], v[156:159], v[216:219], v[96:99]
	v_mfma_f32_16x16x32_bf16 v[88:91], v[164:167], v[216:219], v[88:91]
	v_mfma_f32_16x16x32_bf16 v[80:83], v[156:159], v[224:227], v[80:83]
	v_mfma_f32_16x16x32_bf16 v[72:75], v[164:167], v[224:227], v[72:75]
	s_setprio 0
	s_setprio 1
	v_mfma_f32_16x16x32_bf16 v[124:127], v[168:171], v[184:187], v[124:127]
	v_mfma_f32_16x16x32_bf16 v[116:119], v[176:179], v[184:187], v[116:119]
	v_mfma_f32_16x16x32_bf16 v[108:111], v[168:171], v[192:195], v[108:111]
	v_mfma_f32_16x16x32_bf16 v[100:103], v[176:179], v[192:195], v[100:103]
	v_mfma_f32_16x16x32_bf16 v[92:95], v[168:171], v[212:215], v[92:95]
	v_mfma_f32_16x16x32_bf16 v[84:87], v[176:179], v[212:215], v[84:87]
	v_mfma_f32_16x16x32_bf16 v[76:79], v[168:171], v[220:223], v[76:79]
	v_mfma_f32_16x16x32_bf16 v[68:71], v[176:179], v[220:223], v[68:71]
	v_mfma_f32_16x16x32_bf16 v[124:127], v[172:175], v[188:191], v[124:127]
	v_mfma_f32_16x16x32_bf16 v[116:119], v[180:183], v[188:191], v[116:119]
	v_mfma_f32_16x16x32_bf16 v[108:111], v[172:175], v[196:199], v[108:111]
	v_mfma_f32_16x16x32_bf16 v[100:103], v[180:183], v[196:199], v[100:103]
	v_mfma_f32_16x16x32_bf16 v[92:95], v[172:175], v[216:219], v[92:95]
	v_mfma_f32_16x16x32_bf16 v[84:87], v[180:183], v[216:219], v[84:87]
	v_mfma_f32_16x16x32_bf16 v[76:79], v[172:175], v[224:227], v[76:79]
	v_mfma_f32_16x16x32_bf16 v[68:71], v[180:183], v[224:227], v[68:71]
	s_setprio 0
	s_barrier
; #define PG8_STAGE(bufoff, gbase, voff) do { _Pragma("unroll") for (int _i = 0; _i < 2; ++_i) \
;         __builtin_amdgcn_global_load_lds((const unsigned*)((const char*)(gbase) + (voff)[_i]), (PG8_LAS unsigned*)(lds + (bufoff) + ldsw + _i * 8192), 16, 0, 0); } while (0)
; #define PG8_LDA(dst, b, h) do { _Pragma("unroll") for (int m = 0; m < 4; ++m) _Pragma("unroll") for (int k = 0; k < 2; ++k) dst[m][k] = *(const PG8_LAS bf16x8*)(lds + PG8_SA(b, h) + aoff + m * 2048 + k * 1024); } while (0)
; #define PG8_MMA(ai, bj, At, Bt) do { __builtin_amdgcn_s_setprio(1); _Pragma("unroll") for (int m = 0; m < 4; ++m) _Pragma("unroll") for (int n = 0; n < 2; ++n) _Pragma("unroll") for (int k = 0; k < 2; ++k) \
;         acc[ai][bj][m][n] = __builtin_amdgcn_mfma_f32_16x16x32_bf16(Bt[n][k], At[m][k], acc[ai][bj][m][n], 0, 0, 0); __builtin_amdgcn_s_setprio(0); } while (0)
; #define PG8_WAIT_V(n) asm volatile("s_waitcnt vmcnt(" #n ")" ::: "memory")
; #define PG8_WAIT_L(n) asm volatile("s_waitcnt lgkmcnt(" #n ")" ::: "memory")
; #define PG8_BAR __builtin_amdgcn_s_barrier()
; #define PG8_SCHED __builtin_amdgcn_sched_barrier(0)
;     __host__ __device__ bool next(int i, Unit& u) const {
;         const long L = (long)i * G + c; if (L >= nwg) return false;
;         int wgid = (int)L; { const int q = nwg / NXCD, r = nwg % NXCD, xcd = wgid % NXCD, off = wgid / NXCD; wgid = (xcd < r ? xcd * (q + 1) : r * (q + 1) + (xcd - r) * q) + off; }
;         const int nig = WGM * nN, gid = wgid / nig, fm = gid * WGM, gsz = (nM - fm) < WGM ? (nM - fm) : WGM;
;         u.pm = fm + ((wgid % nig) % gsz); u.pn = (wgid % nig) / gsz; u.idx = i; return true;
; template <class Epi, class Sched, bool ALIGN_EPI = false, bool SP2 = false>
; __device__ __forceinline__ void gemm_phase(PG8_LAS unsigned char* lds, const Gemm g, const Sched& S, const Epi& E, const int tid) {
;     ...
;             PG8_LDA(At, 1, 1); PG8_STAGE(PG8_SB(1, 0), b3, voffB); PG8_STAGE(PG8_SB(1, 1), b3, voffB1); PG8_STAGE(PG8_SA(1, 0), a3, voffA);
;             PG8_WAIT_V(8); PG8_WAIT_L(0); PG8_BAR; PG8_MMA(1, 0, At, B0); PG8_MMA(1, 1, At, B1); PG8_BAR; PG8_SCHED;
	s_add_i32 s36, s63, s33
	v_lshl_add_u64 v[148:149], v[148:149], 0, s[66:67]
	s_mov_b32 m0, s36
	ds_read_b128 v[184:187], v154 offset:49152
	ds_read_b128 v[188:191], v154 offset:50176
	ds_read_b128 v[192:195], v154 offset:51200
	ds_read_b128 v[196:199], v154 offset:52224
	ds_read_b128 v[212:215], v154 offset:53248
	ds_read_b128 v[216:219], v154 offset:54272
	ds_read_b128 v[220:223], v154 offset:55296
	ds_read_b128 v[224:227], v154 offset:56320
	global_load_lds_dwordx4 v[148:149], off
	v_lshl_add_u64 v[148:149], v[200:201], 0, s[66:67]
	s_add_i32 m0, s36, 0x2000
	s_add_i32 s36, s68, s33
	global_load_lds_dwordx4 v[148:149], off
	v_lshl_add_u64 v[148:149], v[202:203], 0, s[66:67]
	s_mov_b32 m0, s36
	s_nop 0
	global_load_lds_dwordx4 v[148:149], off
	v_lshl_add_u64 v[148:149], v[204:205], 0, s[66:67]
	s_add_i32 m0, s36, 0x2000
	s_nop 0
	global_load_lds_dwordx4 v[148:149], off
	v_lshl_add_u64 v[148:149], v[208:209], 0, s[66:67]
	s_mov_b32 m0, s50
	s_nop 0
	global_load_lds_dwordx4 v[148:149], off
	v_lshl_add_u64 v[148:149], v[210:211], 0, s[66:67]
	s_mov_b32 m0, s51
	s_nop 0
	global_load_lds_dwordx4 v[148:149], off
	s_waitcnt vmcnt(8)
	s_waitcnt lgkmcnt(0)
	s_barrier
	s_setprio 1
	s_waitcnt lgkmcnt(0)
	v_mfma_f32_16x16x32_bf16 v[64:67], v[144:147], v[184:187], v[64:67]
	s_add_i32 s55, s55, 1
	s_mul_i32 s2, s55, s54
	s_mul_hi_u32 s3, s55, s88
	v_mfma_f32_16x16x32_bf16 v[56:59], v[160:163], v[184:187], v[56:59]
	s_add_i32 s3, s3, s2
	s_mul_i32 s2, s55, s88
	s_add_u32 s12, s2, s90
	v_mfma_f32_16x16x32_bf16 v[48:51], v[144:147], v[192:195], v[48:51]
	s_addc_u32 s13, s3, s42
	v_mov_b64_e32 v[242:243], 0xb00
	v_cmp_lt_i64_e64 s[2:3], s[12:13], v[242:243]
	v_mfma_f32_16x16x32_bf16 v[40:43], v[160:163], v[192:195], v[40:43]
	s_ashr_i32 s8, s12, 31
	s_lshr_b32 s8, s8, 29
	s_add_i32 s8, s12, s8
	v_mfma_f32_16x16x32_bf16 v[32:35], v[144:147], v[212:215], v[32:35]
	s_ashr_i32 s9, s8, 3
	s_and_b32 s8, s8, -8
	s_sub_i32 s8, s12, s8
	v_mfma_f32_16x16x32_bf16 v[24:27], v[160:163], v[212:215], v[24:27]
	s_cmp_lt_i32 s8, 0
	s_movk_i32 s10, 0x161
	s_cselect_b32 s10, s10, 0x160
	v_mfma_f32_16x16x32_bf16 v[16:19], v[144:147], v[220:223], v[16:19]
	s_mul_i32 s8, s8, s10
	s_add_i32 s8, s8, s9
	s_mul_hi_i32 s9, s8, 0x2e8ba2e9
	v_mfma_f32_16x16x32_bf16 v[8:11], v[160:163], v[220:223], v[8:11]
	s_lshr_b32 s10, s9, 31
	s_ashr_i32 s9, s9, 5
	s_add_i32 s9, s9, s10
	v_mfma_f32_16x16x32_bf16 v[64:67], v[156:159], v[188:191], v[64:67]
	s_lshl_b32 s10, s9, 3
	s_sub_i32 s11, 0x80, s10
	s_min_i32 s11, s11, 8
	v_mfma_f32_16x16x32_bf16 v[56:59], v[164:167], v[188:191], v[56:59]
	s_abs_i32 s12, s11
	s_sub_i32 s14, 0, s12
	v_mfma_f32_16x16x32_bf16 v[48:51], v[156:159], v[196:199], v[48:51]
	s_mulk_i32 s9, 0xb0
	s_sub_i32 s9, s8, s9
	v_mfma_f32_16x16x32_bf16 v[40:43], v[164:167], v[196:199], v[40:43]
	s_abs_i32 s8, s9
	s_xor_b32 s13, s9, s11
	s_ashr_i32 s13, s13, 31
	v_mfma_f32_16x16x32_bf16 v[32:35], v[156:159], v[216:219], v[32:35]
	s_mov_b32 s56, s55
	v_mfma_f32_16x16x32_bf16 v[24:27], v[164:167], v[216:219], v[24:27]
	s_mov_b32 s15, 0x1fffffc0
	s_mul_i32 s14, s14, s15
	s_mul_hi_u32 s14, s15, s14
	v_mfma_f32_16x16x32_bf16 v[16:19], v[156:159], v[224:227], v[16:19]
	s_add_i32 s15, s15, s14
	s_mul_hi_u32 s14, s8, s15
	s_mul_i32 s15, s14, s12
	v_mfma_f32_16x16x32_bf16 v[8:11], v[164:167], v[224:227], v[8:11]
	s_sub_i32 s8, s8, s15
	s_add_i32 s36, s14, 1
	s_sub_i32 s15, s8, s12
	s_setprio 0
	s_setprio 1
	v_mfma_f32_16x16x32_bf16 v[60:63], v[168:171], v[184:187], v[60:63]
	s_cmp_ge_u32 s8, s12
	s_cselect_b32 s14, s36, s14
	s_cselect_b32 s8, s15, s8
	v_mfma_f32_16x16x32_bf16 v[52:55], v[176:179], v[184:187], v[52:55]
	s_add_i32 s15, s14, 1
	s_cmp_ge_u32 s8, s12
	s_cselect_b32 s8, s15, s14
	v_mfma_f32_16x16x32_bf16 v[44:47], v[168:171], v[192:195], v[44:47]
	s_xor_b32 s8, s8, s13
	s_sub_i32 s8, s8, s13
	s_mul_i32 s11, s8, s11
	v_mfma_f32_16x16x32_bf16 v[36:39], v[176:179], v[192:195], v[36:39]
	s_sub_i32 s9, s9, s11
	s_add_i32 s10, s10, s9
	s_ashr_i32 s11, s10, 31
	v_mfma_f32_16x16x32_bf16 v[28:31], v[168:171], v[212:215], v[28:31]
	s_lshl_b64 s[12:13], s[10:11], 19
	s_add_u32 s12, s38, s12
	s_addc_u32 s13, s39, s13
	v_mfma_f32_16x16x32_bf16 v[20:23], v[176:179], v[212:215], v[20:23]
	s_and_b64 s[14:15], s[2:3], exec
	s_cselect_b32 s11, s13, s47
	s_cselect_b32 s59, s12, s46
	v_mfma_f32_16x16x32_bf16 v[12:15], v[168:171], v[220:223], v[12:15]
	s_ashr_i32 s9, s8, 31
	s_lshl_b64 s[14:15], s[8:9], 19
	s_add_u32 s14, s40, s14
	v_mfma_f32_16x16x32_bf16 v[4:7], v[176:179], v[220:223], v[4:7]
	s_addc_u32 s15, s41, s15
	s_and_b64 s[36:37], s[2:3], exec
	s_cselect_b32 s9, s15, s53
	v_mfma_f32_16x16x32_bf16 v[60:63], v[172:175], v[188:191], v[60:63]
	s_cselect_b32 s60, s14, s52
	s_add_i32 s62, s62, 2
	s_add_u32 s46, s46, 0x100
	v_mfma_f32_16x16x32_bf16 v[52:55], v[180:183], v[188:191], v[52:55]
	s_addc_u32 s47, s47, 0
	s_add_u32 s52, s52, 0x100
	s_addc_u32 s53, s53, 0
	v_mfma_f32_16x16x32_bf16 v[44:47], v[172:175], v[196:199], v[44:47]
	s_add_u32 s36, s46, 0xfffc0080
	s_addc_u32 s37, s47, -1
	s_add_i32 s63, 0, 0x10000
	v_mfma_f32_16x16x32_bf16 v[36:39], v[180:183], v[196:199], v[36:39]
	s_cmp_eq_u32 s62, 12
	s_cselect_b32 s37, s11, s37
	v_mfma_f32_16x16x32_bf16 v[28:31], v[172:175], v[216:219], v[28:31]
	s_cselect_b32 s36, s59, s36
	v_add_u32_e32 v148, s63, v151
	v_mfma_f32_16x16x32_bf16 v[20:23], v[180:183], v[216:219], v[20:23]
	s_cselect_b32 s73, s9, s53
	s_cselect_b32 s72, s60, s52
	v_mfma_f32_16x16x32_bf16 v[12:15], v[172:175], v[224:227], v[12:15]
	s_add_i32 s68, 0, 0x14000
	s_cmp_gt_u32 s62, 13
	v_mfma_f32_16x16x32_bf16 v[4:7], v[180:183], v[224:227], v[4:7]
	s_setprio 0
	s_barrier
	s_cbranch_scc1 .Lpeel_done_727
